# P0: nt (streaming) hint on the once-read input loads of the prologue (x, mem, weights)
# speedup vs baseline: 1.0167x; 1.0097x over previous
; #define GAS __attribute__((address_space(1)))
; __device__ __forceinline__ void p0_colmax_item(const float* W, int ldw, int csrc0, int k0, gu32* cmax, int lane) {
;     const int r8 = lane >> 3, c4 = (lane & 7) * 4; f32x4 v[8];
; #pragma unroll
;     for (int i = 0; i < 8; ++i) v[i] = *(const GAS f32x4*)(W + (size_t)(k0 + 8 * i + r8) * ldw + csrc0 + c4);
;     float m0 = 0.f, m1 = 0.f, m2 = 0.f, m3 = 0.f;
; #pragma unroll
;     for (int i = 0; i < 8; ++i) { m0 = fmaxf(m0, fabsf(v[i].x)); m1 = fmaxf(m1, fabsf(v[i].y)); m2 = fmaxf(m2, fabsf(v[i].z)); m3 = fmaxf(m3, fabsf(v[i].w)); }
; #pragma unroll
;     for (int o = 8; o < 64; o <<= 1) { m0 = fmaxf(m0, __shfl_xor(m0, o)); m1 = fmaxf(m1, __shfl_xor(m1, o)); m2 = fmaxf(m2, __shfl_xor(m2, o)); m3 = fmaxf(m3, __shfl_xor(m3, o)); }
;     if (lane < 8) { unsigned* cm = (unsigned*)(cmax + c4);
;         const unsigned o0 = __hip_atomic_fetch_max(cm + 0, __builtin_bit_cast(unsigned, m0), RLX_AGENT), o1 = __hip_atomic_fetch_max(cm + 1, __builtin_bit_cast(unsigned, m1), RLX_AGENT);
;         const unsigned o2 = __hip_atomic_fetch_max(cm + 2, __builtin_bit_cast(unsigned, m2), RLX_AGENT), o3 = __hip_atomic_fetch_max(cm + 3, __builtin_bit_cast(unsigned, m3), RLX_AGENT);
;         asm volatile("" :: "v"(o0), "v"(o1), "v"(o2), "v"(o3)); }
; }
; __device__ __forceinline__ void p0_prologue(Frame& F, const Args& A) {
;     ...
;         else { const int r = it - I_IN; p0_colmax_item(A.in[14], 2 * D, (r % 64) * 32, (r / 64) * 64, cmax + NP + (r % 64) * 32, lane); }
.LBB0_12:
	s_cmpk_gt_i32 s9, 0x4ff
	s_mov_b64 s[4:5], -1
	s_cbranch_scc0 .LBB0_16
	s_and_b32 s4, s9, 0x7fffffc0
	s_and_b32 s2, s6, 0x7e0
	v_add_u32_e32 v2, s4, v1
	s_lshl_b32 s2, s2, 2
	s_waitcnt lgkmcnt(2)
	v_or_b32_e32 v20, 8, v2
	v_mov_b32_e32 v21, v3
	v_lshl_add_u64 v[42:43], v[8:9], 0, s[2:3]
	v_lshlrev_b64 v[18:19], 13, v[2:3]
	v_lshlrev_b64 v[20:21], 13, v[20:21]
	v_or_b32_e32 v26, 16, v2
	v_mov_b32_e32 v27, v3
	v_or_b32_e32 v28, 24, v2
	v_mov_b32_e32 v29, v3
	v_lshl_add_u64 v[18:19], v[42:43], 0, v[18:19]
	s_waitcnt lgkmcnt(0)
	v_lshl_add_u64 v[22:23], v[42:43], 0, v[20:21]
	v_lshlrev_b64 v[26:27], 13, v[26:27]
	v_lshlrev_b64 v[28:29], 13, v[28:29]
	v_or_b32_e32 v34, 32, v2
	v_mov_b32_e32 v35, v3
	v_or_b32_e32 v36, 40, v2
	v_mov_b32_e32 v37, v3
	global_load_dwordx4 v[18:21], v[18:19], off nt
	s_nop 0
	global_load_dwordx4 v[22:25], v[22:23], off nt
	v_lshl_add_u64 v[26:27], v[42:43], 0, v[26:27]
	v_lshl_add_u64 v[30:31], v[42:43], 0, v[28:29]
	v_lshlrev_b64 v[34:35], 13, v[34:35]
	v_lshlrev_b64 v[36:37], 13, v[36:37]
	v_or_b32_e32 v44, 48, v2
	v_mov_b32_e32 v45, v3
	v_or_b32_e32 v2, 56, v2
	global_load_dwordx4 v[26:29], v[26:27], off nt
	s_nop 0
	global_load_dwordx4 v[30:33], v[30:31], off nt
	v_lshl_add_u64 v[34:35], v[42:43], 0, v[34:35]
	v_lshl_add_u64 v[38:39], v[42:43], 0, v[36:37]
	v_lshlrev_b64 v[44:45], 13, v[44:45]
	v_lshlrev_b64 v[46:47], 13, v[2:3]
	global_load_dwordx4 v[34:37], v[34:35], off nt
	s_nop 0
	global_load_dwordx4 v[38:41], v[38:39], off nt
	v_lshl_add_u64 v[44:45], v[42:43], 0, v[44:45]
	v_lshl_add_u64 v[46:47], v[42:43], 0, v[46:47]
	global_load_dwordx4 v[42:45], v[44:45], off nt
	s_nop 0
	global_load_dwordx4 v[46:49], v[46:47], off nt
	v_cmp_lt_i32_e32 vcc, v14, v13
	s_waitcnt vmcnt(6)
	v_max3_f32 v18, |v18|, 0, |v22|
	v_max3_f32 v19, |v19|, 0, |v23|
	v_max3_f32 v20, |v20|, 0, |v24|
	v_max3_f32 v21, |v21|, 0, |v25|
	v_cndmask_b32_e32 v2, v12, v14, vcc
	v_lshlrev_b32_e32 v2, 2, v2
	v_cmp_lt_i32_e32 vcc, v15, v13
	s_waitcnt vmcnt(4)
	v_max3_f32 v18, v18, |v26|, |v30|
	v_max3_f32 v19, v19, |v27|, |v31|
	v_max3_f32 v20, v20, |v28|, |v32|
	v_max3_f32 v21, v21, |v29|, |v33|
	v_cndmask_b32_e32 v17, v12, v15, vcc
	s_waitcnt vmcnt(2)
	v_max3_f32 v18, v18, |v34|, |v38|
	v_max3_f32 v19, v19, |v35|, |v39|
	v_max3_f32 v20, v20, |v36|, |v40|
	v_max3_f32 v21, v21, |v37|, |v41|
	s_waitcnt vmcnt(0)
	v_max3_f32 v18, v18, |v42|, |v46|
	v_max3_f32 v19, v19, |v43|, |v47|
	v_max3_f32 v20, v20, |v44|, |v48|
	v_max3_f32 v21, v21, |v45|, |v49|
	ds_bpermute_b32 v22, v2, v18
	ds_bpermute_b32 v23, v2, v19
	ds_bpermute_b32 v24, v2, v20
	ds_bpermute_b32 v2, v2, v21
	v_lshlrev_b32_e32 v17, 2, v17
	s_waitcnt lgkmcnt(3)
	v_max_f32_e32 v22, v22, v22
	s_waitcnt lgkmcnt(2)
	v_max_f32_e32 v23, v23, v23
	s_waitcnt lgkmcnt(1)
	v_max_f32_e32 v24, v24, v24
	s_waitcnt lgkmcnt(0)
	v_max_f32_e32 v2, v2, v2
	v_max_f32_e32 v18, v18, v22
	v_max_f32_e32 v19, v19, v23
	v_max_f32_e32 v20, v20, v24
	v_max_f32_e32 v21, v21, v2
	ds_bpermute_b32 v2, v17, v18
	ds_bpermute_b32 v22, v17, v19
	ds_bpermute_b32 v23, v17, v20
	ds_bpermute_b32 v17, v17, v21
	v_cmp_lt_i32_e32 vcc, v16, v13
	s_waitcnt lgkmcnt(3)
	v_max_f32_e32 v2, v2, v2
	s_waitcnt lgkmcnt(2)
	v_max_f32_e32 v22, v22, v22
	v_cndmask_b32_e32 v50, v12, v16, vcc
	s_waitcnt lgkmcnt(1)
	v_max_f32_e32 v23, v23, v23
	s_waitcnt lgkmcnt(0)
	v_max_f32_e32 v25, v17, v17
	v_lshlrev_b32_e32 v24, 2, v50
	v_max_f32_e32 v2, v18, v2
	v_max_f32_e32 v17, v19, v22
	v_max_f32_e32 v19, v20, v23
	v_max_f32_e32 v21, v21, v25
	ds_bpermute_b32 v18, v24, v2
	ds_bpermute_b32 v20, v24, v17
	ds_bpermute_b32 v22, v24, v19
	ds_bpermute_b32 v23, v24, v21
	s_and_saveexec_b64 s[4:5], s[0:1]
	s_cbranch_execz .LBB0_15
	s_waitcnt lgkmcnt(1)
	v_max_f32_e32 v22, v22, v22
	v_max_f32_e32 v19, v19, v19
	v_max_f32_e32 v22, v19, v22
	v_max_f32_e32 v19, v20, v20
	v_max_f32_e32 v17, v17, v17
	v_max_f32_e32 v18, v18, v18
	v_max_f32_e32 v2, v2, v2
	s_waitcnt lgkmcnt(0)
	v_max_f32_e32 v23, v23, v23
	v_max_f32_e32 v21, v21, v21
	v_max_f32_e32 v17, v17, v19
	v_max_f32_e32 v2, v2, v18
	v_lshl_add_u64 v[18:19], v[4:5], 0, s[2:3]
	v_max_f32_e32 v21, v21, v23
	global_atomic_umax v2, v[18:19], v2, off sc0
	s_nop 0
	global_atomic_umax v17, v[18:19], v17, off offset:4 sc0
	s_nop 0
	global_atomic_umax v20, v[18:19], v22, off offset:8 sc0
	s_nop 0
	global_atomic_umax v18, v[18:19], v21, off offset:12 sc0
	s_waitcnt vmcnt(0)

; #define GAS __attribute__((address_space(1)))
; __device__ __forceinline__ void p0_colmax_item(const float* W, int ldw, int csrc0, int k0, gu32* cmax, int lane) {
;     const int r8 = lane >> 3, c4 = (lane & 7) * 4; f32x4 v[8];
; #pragma unroll
;     for (int i = 0; i < 8; ++i) v[i] = *(const GAS f32x4*)(W + (size_t)(k0 + 8 * i + r8) * ldw + csrc0 + c4);
;     float m0 = 0.f, m1 = 0.f, m2 = 0.f, m3 = 0.f;
; #pragma unroll
;     for (int i = 0; i < 8; ++i) { m0 = fmaxf(m0, fabsf(v[i].x)); m1 = fmaxf(m1, fabsf(v[i].y)); m2 = fmaxf(m2, fabsf(v[i].z)); m3 = fmaxf(m3, fabsf(v[i].w)); }
; #pragma unroll
;     for (int o = 8; o < 64; o <<= 1) { m0 = fmaxf(m0, __shfl_xor(m0, o)); m1 = fmaxf(m1, __shfl_xor(m1, o)); m2 = fmaxf(m2, __shfl_xor(m2, o)); m3 = fmaxf(m3, __shfl_xor(m3, o)); }
;     if (lane < 8) { unsigned* cm = (unsigned*)(cmax + c4);
;         const unsigned o0 = __hip_atomic_fetch_max(cm + 0, __builtin_bit_cast(unsigned, m0), RLX_AGENT), o1 = __hip_atomic_fetch_max(cm + 1, __builtin_bit_cast(unsigned, m1), RLX_AGENT);
;         const unsigned o2 = __hip_atomic_fetch_max(cm + 2, __builtin_bit_cast(unsigned, m2), RLX_AGENT), o3 = __hip_atomic_fetch_max(cm + 3, __builtin_bit_cast(unsigned, m3), RLX_AGENT);
;         asm volatile("" :: "v"(o0), "v"(o1), "v"(o2), "v"(o3)); }
; }
; __device__ __forceinline__ void p0_prologue(Frame& F, const Args& A) {
;     ...
;         if (it < I_IN) { const int kb = it / (NP / 32), nb = it % (NP / 32), n0 = nb * 32; p0_colmax_item(A.in[3], INW, n0 + (n0 >= 1536 ? 8 : 0), kb * 64, cmax + n0, lane); }
.LBB0_17:
	s_mul_hi_i32 s2, s9, 0x66666667
	s_lshr_b32 s4, s2, 31
	s_ashr_i32 s2, s2, 5
	s_add_i32 s5, s2, s4
	s_mul_i32 s2, s5, 0xffffffb0
	s_add_i32 s4, s9, s2
	s_cmp_gt_i32 s4, 47
	s_cselect_b32 s4, 8, 0
	s_mul_i32 s2, s5, 0xfffff600
	s_add_i32 s4, s4, s6
	s_add_i32 s4, s4, s2
	v_lshl_or_b32 v2, s5, 6, v167
	s_ashr_i32 s5, s4, 31
	v_lshl_add_u64 v[42:43], s[4:5], 2, v[10:11]
	v_or_b32_e32 v17, 8, v2
	s_waitcnt lgkmcnt(0)
	v_mad_i64_i32 v[22:23], s[4:5], v17, s8, v[42:43]
	v_or_b32_e32 v17, 16, v2
	v_mad_i64_i32 v[26:27], s[4:5], v17, s8, v[42:43]
	v_or_b32_e32 v17, 24, v2
	v_mad_i64_i32 v[18:19], s[4:5], v2, s8, v[42:43]
	v_mad_i64_i32 v[30:31], s[4:5], v17, s8, v[42:43]
	v_or_b32_e32 v17, 32, v2
	global_load_dwordx4 v[18:21], v[18:19], off nt
	s_nop 0
	global_load_dwordx4 v[22:25], v[22:23], off nt
	v_mad_i64_i32 v[34:35], s[4:5], v17, s8, v[42:43]
	v_or_b32_e32 v17, 40, v2
	global_load_dwordx4 v[26:29], v[26:27], off nt
	s_nop 0
	global_load_dwordx4 v[30:33], v[30:31], off nt
	v_mad_i64_i32 v[38:39], s[4:5], v17, s8, v[42:43]
	v_or_b32_e32 v17, 48, v2
	v_or_b32_e32 v2, 56, v2
	global_load_dwordx4 v[34:37], v[34:35], off nt
	s_nop 0
	global_load_dwordx4 v[38:41], v[38:39], off nt
	v_mad_i64_i32 v[44:45], s[4:5], v17, s8, v[42:43]
	v_mad_i64_i32 v[46:47], s[4:5], v2, s8, v[42:43]
	global_load_dwordx4 v[42:45], v[44:45], off nt
	s_nop 0
	global_load_dwordx4 v[46:49], v[46:47], off nt
	v_cmp_lt_i32_e32 vcc, v14, v13
	s_waitcnt vmcnt(6)
	v_max3_f32 v18, |v18|, 0, |v22|
	v_max3_f32 v19, |v19|, 0, |v23|
	v_max3_f32 v20, |v20|, 0, |v24|
	v_max3_f32 v21, |v21|, 0, |v25|
	s_waitcnt vmcnt(4)
	v_max3_f32 v18, v18, |v26|, |v30|
	v_max3_f32 v19, v19, |v27|, |v31|
	v_max3_f32 v20, v20, |v28|, |v32|
	v_max3_f32 v21, v21, |v29|, |v33|
	v_cndmask_b32_e32 v2, v12, v14, vcc
	s_waitcnt vmcnt(2)
	v_max3_f32 v18, v18, |v34|, |v38|
	v_max3_f32 v19, v19, |v35|, |v39|
	v_max3_f32 v20, v20, |v36|, |v40|
	v_max3_f32 v21, v21, |v37|, |v41|
	v_lshlrev_b32_e32 v2, 2, v2
	s_waitcnt vmcnt(0)
	v_max3_f32 v18, v18, |v42|, |v46|
	v_max3_f32 v19, v19, |v43|, |v47|
	v_max3_f32 v20, v20, |v44|, |v48|
	v_max3_f32 v21, v21, |v45|, |v49|
	ds_bpermute_b32 v22, v2, v18
	ds_bpermute_b32 v23, v2, v19
	ds_bpermute_b32 v24, v2, v20
	ds_bpermute_b32 v2, v2, v21
	v_cmp_lt_i32_e32 vcc, v15, v13
	s_waitcnt lgkmcnt(3)
	v_max_f32_e32 v22, v22, v22
	s_waitcnt lgkmcnt(2)
	v_max_f32_e32 v23, v23, v23
	v_cndmask_b32_e32 v17, v12, v15, vcc
	s_waitcnt lgkmcnt(1)
	v_max_f32_e32 v24, v24, v24
	s_waitcnt lgkmcnt(0)
	v_max_f32_e32 v2, v2, v2
	v_lshlrev_b32_e32 v17, 2, v17
	v_max_f32_e32 v18, v18, v22
	v_max_f32_e32 v19, v19, v23
	v_max_f32_e32 v20, v20, v24
	v_max_f32_e32 v21, v21, v2
	ds_bpermute_b32 v2, v17, v18
	ds_bpermute_b32 v22, v17, v19
	ds_bpermute_b32 v23, v17, v20
	ds_bpermute_b32 v17, v17, v21
	v_cmp_lt_i32_e32 vcc, v16, v13
	s_waitcnt lgkmcnt(3)
	v_max_f32_e32 v2, v2, v2
	s_waitcnt lgkmcnt(2)
	v_max_f32_e32 v22, v22, v22
	v_cndmask_b32_e32 v50, v12, v16, vcc
	s_waitcnt lgkmcnt(1)
	v_max_f32_e32 v23, v23, v23
	s_waitcnt lgkmcnt(0)
	v_max_f32_e32 v25, v17, v17
	v_lshlrev_b32_e32 v24, 2, v50
	v_max_f32_e32 v2, v18, v2
	v_max_f32_e32 v17, v19, v22
	v_max_f32_e32 v19, v20, v23
	v_max_f32_e32 v21, v21, v25
	ds_bpermute_b32 v18, v24, v2
	ds_bpermute_b32 v20, v24, v17
	ds_bpermute_b32 v22, v24, v19
	ds_bpermute_b32 v23, v24, v21
	s_and_saveexec_b64 s[4:5], s[0:1]
	s_cbranch_execz .LBB0_10
	s_add_i32 s10, s6, s2
	s_waitcnt lgkmcnt(1)
	v_max_f32_e32 v22, v22, v22
	v_max_f32_e32 v19, v19, v19
	s_ashr_i32 s11, s10, 31
	v_max_f32_e32 v22, v19, v22
	v_max_f32_e32 v19, v20, v20
	v_max_f32_e32 v17, v17, v17
	v_max_f32_e32 v18, v18, v18
	v_max_f32_e32 v2, v2, v2
	s_waitcnt lgkmcnt(0)
	v_max_f32_e32 v23, v23, v23
	v_max_f32_e32 v21, v21, v21
	v_max_f32_e32 v17, v17, v19
	v_max_f32_e32 v2, v2, v18
	v_lshl_add_u64 v[18:19], s[10:11], 2, v[6:7]
	v_max_f32_e32 v21, v21, v23
	global_atomic_umax v2, v[18:19], v2, off sc0
	s_nop 0
	global_atomic_umax v17, v[18:19], v17, off offset:4 sc0
	s_nop 0
	global_atomic_umax v20, v[18:19], v22, off offset:8 sc0
	s_nop 0
	global_atomic_umax v18, v[18:19], v21, off offset:12 sc0
	s_waitcnt vmcnt(0)
	s_branch .LBB0_10

; #define GAS __attribute__((address_space(1)))
; __device__ __forceinline__ void p0_prologue(Frame& F, const Args& A) {
;     ...
;             for (int rr = 0; rr < 2; ++rr) { const int m = m0 + rr * NGW; const GAS f32x4* xr = (const GAS f32x4*)(x + (size_t)(m < T ? m : m0) * D) + lane;
; #pragma unroll
;                 for (int j = 0; j < 4; ++j) vv[rr][j] = xr[64 * j]; }
.LBB0_34:
	s_ashr_i32 s21, s20, 31
	s_lshl_b64 s[12:13], s[20:21], 12
	v_lshl_add_u64 v[146:147], v[172:173], 0, s[12:13]
	global_load_dwordx4 v[178:181], v[146:147], off nt
	global_load_dwordx4 v[182:185], v[146:147], off offset:1024 nt
	global_load_dwordx4 v[208:211], v[146:147], off offset:2048 nt
	global_load_dwordx4 v[212:215], v[146:147], off offset:3072 nt
	s_add_i32 s95, s20, s34
	s_cmp_lt_i32 s95, 0x10000
	s_cselect_b64 s[66:67], -1, 0
	s_and_b64 s[12:13], s[66:67], exec
	s_cselect_b32 s24, s95, s20
	s_ashr_i32 s25, s24, 31
	s_lshl_b64 s[12:13], s[24:25], 12
	v_lshl_add_u64 v[146:147], v[172:173], 0, s[12:13]
	global_load_dwordx4 v[158:161], v[146:147], off nt
	global_load_dwordx4 v[154:157], v[146:147], off offset:1024 nt
	global_load_dwordx4 v[150:153], v[146:147], off offset:2048 nt
	s_nop 0
	global_load_dwordx4 v[146:149], v[146:147], off offset:3072 nt
	s_waitcnt vmcnt(7)
	v_pk_mul_f32 v[186:187], v[180:181], v[180:181]
	v_pk_mul_f32 v[188:189], v[178:179], v[178:179]
	s_waitcnt vmcnt(4)
; #define GAS __attribute__((address_space(1)))
; __device__ __forceinline__ void p0_prologue(Frame& F, const Args& A) {
;     ...
;             for (int rr = 0; rr < 2; ++rr) { const int mraw = m0 + rr * NGW; const bool mvalid = mraw < T; const int m = mvalid ? mraw : m0;
;                 f32x4 v[4]; float s = 0.f;
; #pragma unroll
;                 for (int j = 0; j < 4; ++j) { v[j] = vv[rr][j]; s += (v[j].x * v[j].x + v[j].y * v[j].y) + (v[j].z * v[j].z + v[j].w * v[j].w); }
;                 const float r = rsqrtf(wave_sum(s) * (1.f / D) + EPS);
; #pragma unroll
;                 for (int j = 0; j < 4; ++j) v[j] = v[j] * r * g[j];
;                 { float mx = 0.f;
; #pragma unroll
;                   for (int j = 0; j < 4; ++j) mx = fmaxf(fmaxf(mx, fmaxf(fabsf(v[j].x), fabsf(v[j].y))), fmaxf(fabsf(v[j].z), fabsf(v[j].w)));
;                   mx = wave_max(mx); const float qs = mx > 0.f ? 127.0f / mx : 0.f;
;                   GAS unsigned* o4 = (GAS unsigned*)(xn + (size_t)m * D) + lane;
;                   if (mvalid) {
; #pragma unroll
;                   for (int j = 0; j < 4; ++j) o4[64 * j] = pk4_i8s(v[j].x, v[j].y, v[j].z, v[j].w, qs);
;                   if (lane == 0) rsc[m] = mx * (1.0f / 127.0f); } }
	v_mul_f32_e32 v177, v212, v212
	v_pk_mov_b32 v[190:191], v[188:189], v[186:187] op_sel:[1,0]
	v_mov_b32_e32 v189, v187
	v_pk_add_f32 v[186:187], v[190:191], v[188:189]
	v_pk_mul_f32 v[188:189], v[184:185], v[184:185]
	v_pk_mul_f32 v[190:191], v[182:183], v[182:183]
	v_pk_add_f32 v[186:187], v[186:187], v[186:187] op_sel:[0,1] op_sel_hi:[1,0]
	v_pk_mov_b32 v[192:193], v[190:191], v[188:189] op_sel:[1,0]
	v_mov_b32_e32 v191, v189
	v_pk_add_f32 v[188:189], v[192:193], v[190:191]
	v_mul_f32_e32 v190, v213, v213
	v_pk_add_f32 v[188:189], v[188:189], v[188:189] op_sel:[0,1] op_sel_hi:[1,0]
	v_mov_b32_e32 v187, v177
	v_mov_b32_e32 v189, v190
	v_pk_add_f32 v[186:187], v[186:187], v[188:189]
	v_mul_f32_e32 v188, v209, v209
	v_mul_f32_e32 v191, v214, v214
	v_pk_fma_f32 v[188:189], v[208:209], v[208:209], v[188:189] op_sel_hi:[1,1,0]
	v_mul_f32_e32 v190, v211, v211
	v_mul_f32_e32 v192, v215, v215
	v_mov_b32_e32 v189, v191
	v_pk_fma_f32 v[190:191], v[210:211], v[210:211], v[190:191] op_sel_hi:[1,1,0]
	s_nop 0
	v_mov_b32_e32 v191, v192
	v_pk_add_f32 v[188:189], v[188:189], v[190:191]
	s_nop 0
	v_pk_add_f32 v[186:187], v[186:187], v[188:189]
	s_nop 0
	v_add_f32_e32 v177, v186, v187
	s_nop 1
	v_add_f32_dpp v177, v177, v177 row_ror:1 row_mask:0xf bank_mask:0xf bound_ctrl:1
	s_nop 1
	v_add_f32_dpp v177, v177, v177 row_ror:2 row_mask:0xf bank_mask:0xf bound_ctrl:1
	s_nop 1
	v_add_f32_dpp v177, v177, v177 row_ror:4 row_mask:0xf bank_mask:0xf bound_ctrl:1
	s_nop 1
	v_add_f32_dpp v177, v177, v177 row_ror:8 row_mask:0xf bank_mask:0xf bound_ctrl:1
	s_nop 0
	v_readlane_b32 vcc_lo, v177, 16
	v_readlane_b32 vcc_hi, v177, 48
	v_readlane_b32 s12, v177, 0
	v_readlane_b32 s13, v177, 32
	v_mov_b32_e32 v186, vcc_lo
	v_mov_b32_e32 v187, vcc_hi
	v_pk_add_f32 v[186:187], s[12:13], v[186:187]
	s_nop 0
	v_add_f32_e32 v177, v186, v187
	v_fmamk_f32 v177, v177, 0x3a800000, v165
	v_cmp_gt_f32_e32 vcc, s72, v177
	v_mul_f32_e32 v186, 0x4b800000, v177
	s_nop 0
	v_cndmask_b32_e32 v177, v177, v186, vcc
	v_rsq_f32_e32 v177, v177
	s_nop 0
	v_mul_f32_e32 v186, 0x45800000, v177
	v_cndmask_b32_e32 v194, v177, v186, vcc
	v_pk_mul_f32 v[178:179], v[178:179], v[194:195] op_sel_hi:[1,0]
	v_pk_mul_f32 v[180:181], v[180:181], v[194:195] op_sel_hi:[1,0]
	v_pk_mul_f32 v[192:193], v[2:3], v[178:179]
	v_pk_mul_f32 v[178:179], v[182:183], v[194:195] op_sel_hi:[1,0]
	v_pk_mul_f32 v[188:189], v[4:5], v[180:181]
	v_pk_mul_f32 v[180:181], v[184:185], v[194:195] op_sel_hi:[1,0]
	v_pk_mul_f32 v[190:191], v[6:7], v[178:179]
	v_pk_mul_f32 v[178:179], v[208:209], v[194:195] op_sel_hi:[1,0]
	v_pk_mul_f32 v[184:185], v[8:9], v[180:181]
	v_pk_mul_f32 v[180:181], v[210:211], v[194:195] op_sel_hi:[1,0]
	v_pk_mul_f32 v[186:187], v[10:11], v[178:179]
	v_pk_mul_f32 v[182:183], v[212:213], v[194:195] op_sel_hi:[1,0]
	v_pk_mul_f32 v[178:179], v[214:215], v[194:195] op_sel_hi:[1,0]
	v_max_f32_e64 v177, |v192|, |v193|
	v_max_f32_e64 v194, |v188|, |v189|
	v_pk_mul_f32 v[180:181], v[12:13], v[180:181]
	v_max3_f32 v177, v177, 0, v194
	v_max_f32_e64 v194, |v190|, |v191|
	v_max_f32_e64 v195, |v184|, |v185|
	v_pk_mul_f32 v[178:179], v[16:17], v[178:179]
	v_pk_mul_f32 v[182:183], v[14:15], v[182:183]
	v_max3_f32 v177, v177, v194, v195
	v_max_f32_e64 v194, |v186|, |v187|
	v_max_f32_e64 v195, |v180|, |v181|
	v_max3_f32 v177, v177, v194, v195
	v_max_f32_e64 v194, |v182|, |v183|
	v_max_f32_e64 v195, |v178|, |v179|
	v_max3_f32 v177, v177, v194, v195
	v_mov_b32_e32 v194, 0
	s_nop 1
	v_mov_b32_dpp v194, v177 row_ror:1 row_mask:0xf bank_mask:0xf
	v_max_f32_e32 v194, v194, v194
	v_max_f32_e32 v177, v177, v194
	v_mov_b32_e32 v194, 0
	s_nop 1
	v_mov_b32_dpp v194, v177 row_ror:2 row_mask:0xf bank_mask:0xf
	v_max_f32_e32 v194, v194, v194
	v_max_f32_e32 v177, v177, v194
	v_mov_b32_e32 v194, 0
	s_nop 1
	v_mov_b32_dpp v194, v177 row_ror:4 row_mask:0xf bank_mask:0xf
	v_max_f32_e32 v194, v194, v194
	v_max_f32_e32 v177, v177, v194
	v_mov_b32_e32 v194, 0
	s_nop 1
	v_mov_b32_dpp v194, v177 row_ror:8 row_mask:0xf bank_mask:0xf
	v_max_f32_e32 v194, v194, v194
	v_max_f32_e32 v177, v177, v194
	s_nop 0
	v_readlane_b32 vcc_lo, v177, 32
	v_readlane_b32 vcc_hi, v177, 48
	v_readlane_b32 s12, v177, 0
	v_readlane_b32 s13, v177, 16
	v_max_f32_e64 v177, vcc_hi, vcc_hi
	v_max_f32_e64 v194, vcc_lo, vcc_lo
	v_max_f32_e32 v177, v194, v177
	v_mov_b32_e32 v194, s13
	v_max3_f32 v177, s12, v194, v177
	v_div_scale_f32 v207, vcc, v177, v177, s73
	v_rcp_f32_e32 v208, v207
	s_lshl_b64 s[12:13], s[20:21], 10
	v_lshl_add_u64 v[194:195], v[174:175], 0, s[12:13]
	v_cmp_lt_f32_e64 s[12:13], 0, v177
	v_fma_f32 v209, -v207, v208, 1.0
	v_fmac_f32_e32 v208, v209, v208
	v_div_scale_f32 v209, vcc, s73, v177, s73
	v_mul_f32_e32 v210, v209, v208
	v_fma_f32 v211, -v207, v210, v209
	v_fmac_f32_e32 v210, v211, v208
	v_fma_f32 v207, -v207, v210, v209
	v_div_fmas_f32 v207, v207, v208, v210
	v_div_fixup_f32 v207, v207, v177, s73
	v_cndmask_b32_e64 v207, 0, v207, s[12:13]
	v_fmaak_f32 v208, v192, v207, 0x4b400000
	v_fmaak_f32 v209, v193, v207, 0x4b400000
	v_fmaak_f32 v210, v188, v207, 0x4b400000
	v_fmaak_f32 v211, v189, v207, 0x4b400000
	v_perm_b32 v210, v211, v210, s74
	v_perm_b32 v208, v209, v208, s74
	v_perm_b32 v208, v210, v208, s75
	global_store_dword v[194:195], v208, off
	v_fmaak_f32 v208, v190, v207, 0x4b400000
	v_fmaak_f32 v209, v191, v207, 0x4b400000
	v_fmaak_f32 v210, v184, v207, 0x4b400000
	v_fmaak_f32 v211, v185, v207, 0x4b400000
	v_perm_b32 v210, v211, v210, s74
	v_perm_b32 v208, v209, v208, s74
	v_perm_b32 v208, v210, v208, s75
	global_store_dword v[194:195], v208, off offset:256
	v_fmaak_f32 v208, v186, v207, 0x4b400000
	v_fmaak_f32 v209, v187, v207, 0x4b400000
	v_fmaak_f32 v210, v180, v207, 0x4b400000
	v_fmaak_f32 v211, v181, v207, 0x4b400000
	v_perm_b32 v210, v211, v210, s74
	v_perm_b32 v208, v209, v208, s74
	v_perm_b32 v208, v210, v208, s75
	global_store_dword v[194:195], v208, off offset:512
	v_fmaak_f32 v208, v182, v207, 0x4b400000
	v_fmaak_f32 v209, v183, v207, 0x4b400000
	v_fmaak_f32 v210, v178, v207, 0x4b400000
	v_fmaak_f32 v207, v179, v207, 0x4b400000
	v_perm_b32 v207, v207, v210, s74
	v_perm_b32 v208, v209, v208, s74
	v_perm_b32 v207, v207, v208, s75
	global_store_dword v[194:195], v207, off offset:768
	s_and_saveexec_b64 s[12:13], s[2:3]
	s_cbranch_execz .LBB0_36
	s_lshl_b64 vcc, s[20:21], 2
	s_add_u32 vcc_lo, s35, vcc_lo
	v_mul_f32_e32 v177, 0x3c010204, v177
	s_addc_u32 vcc_hi, s70, vcc_hi
	global_store_dword v163, v177, vcc

; #define GAS __attribute__((address_space(1)))
; __device__ __forceinline__ void p0_prologue(Frame& F, const Args& A) {
;     ...
;         for (int m = gw; m < TM; m += NGW) {
;             const GAS f32x4* xr = (const GAS f32x4*)(x + (size_t)m * D) + lane;
;             f32x4 v[4]; float s = 0.f;
; #pragma unroll
;             for (int j = 0; j < 4; ++j) { v[j] = xr[64 * j]; s += (v[j].x * v[j].x + v[j].y * v[j].y) + (v[j].z * v[j].z + v[j].w * v[j].w); }
;             const float r = rsqrtf(wave_sum(s) * (1.f / D) + EPS);
; #pragma unroll
;             for (int j = 0; j < 4; ++j) v[j] = v[j] * r * g[j];
;             float mx = 0.f;
; #pragma unroll
;             for (int j = 0; j < 4; ++j) mx = fmaxf(fmaxf(mx, fmaxf(fabsf(v[j].x), fabsf(v[j].y))), fmaxf(fabsf(v[j].z), fabsf(v[j].w)));
;             mx = wave_max(mx); const float qs = mx > 0.f ? 127.0f / mx : 0.f;
;             GAS unsigned* o4 = (GAS unsigned*)(mn + (size_t)m * D) + lane;
; #pragma unroll
;             for (int j = 0; j < 4; ++j) o4[64 * j] = pk4_i8s(v[j].x, v[j].y, v[j].z, v[j].w, qs);
;             if (lane == 0) ((float*)(ws + WS_SAM))[m] = mx * (1.0f / 127.0f);
;         }
.LBB0_51:
	global_load_dwordx4 v[22:25], v[20:21], off offset:-3072 nt
	global_load_dwordx4 v[26:29], v[20:21], off offset:-2048 nt
	global_load_dwordx4 v[30:33], v[20:21], off nt
	global_load_dwordx4 v[34:37], v[20:21], off offset:-1024 nt
	v_mov_b32_e32 v49, 0
	v_mov_b32_e32 v52, 0
	s_waitcnt vmcnt(3)
	v_pk_mul_f32 v[38:39], v[24:25], v[24:25]
	v_pk_mul_f32 v[40:41], v[22:23], v[22:23]
	s_waitcnt vmcnt(2)
	v_pk_mul_f32 v[42:43], v[28:29], v[28:29]
	v_pk_mul_f32 v[44:45], v[26:27], v[26:27]
	v_pk_mov_b32 v[50:51], v[40:41], v[38:39] op_sel:[1,0]
	v_mov_b32_e32 v41, v39
	v_pk_mov_b32 v[38:39], v[44:45], v[42:43] op_sel:[1,0]
	v_mov_b32_e32 v45, v43
	s_waitcnt vmcnt(0)
	v_mul_f32_e32 v46, v35, v35
	v_mul_f32_e32 v48, v37, v37
	v_pk_add_f32 v[40:41], v[50:51], v[40:41]
	v_pk_add_f32 v[38:39], v[38:39], v[44:45]
	v_mul_f32_e32 v53, v30, v30
	v_mul_f32_e32 v54, v31, v31
	v_mul_f32_e32 v55, v32, v32
	v_mul_f32_e32 v56, v33, v33
	v_pk_fma_f32 v[42:43], v[34:35], v[34:35], v[46:47] op_sel_hi:[1,1,0]
	v_pk_fma_f32 v[46:47], v[36:37], v[36:37], v[48:49] op_sel_hi:[1,1,0]
	v_pk_add_f32 v[40:41], v[40:41], v[40:41] op_sel:[0,1] op_sel_hi:[1,0]
	v_pk_add_f32 v[38:39], v[38:39], v[38:39] op_sel:[0,1] op_sel_hi:[1,0]
	v_mov_b32_e32 v43, v55
	v_mov_b32_e32 v47, v56
	v_mov_b32_e32 v41, v53
	v_mov_b32_e32 v39, v54
	v_pk_add_f32 v[42:43], v[42:43], v[46:47]
	v_pk_add_f32 v[38:39], v[40:41], v[38:39]
	s_nop 0
	v_pk_add_f32 v[38:39], v[38:39], v[42:43]
	v_mov_b32_e32 v42, 0
	v_add_f32_e32 v38, v38, v39
	v_mov_b32_e32 v43, 0
	s_nop 0
	v_add_f32_dpp v38, v38, v38 row_ror:1 row_mask:0xf bank_mask:0xf bound_ctrl:1
	s_nop 1
	v_add_f32_dpp v38, v38, v38 row_ror:2 row_mask:0xf bank_mask:0xf bound_ctrl:1
	s_nop 1
	v_add_f32_dpp v38, v38, v38 row_ror:4 row_mask:0xf bank_mask:0xf bound_ctrl:1
	s_nop 1
	v_add_f32_dpp v38, v38, v38 row_ror:8 row_mask:0xf bank_mask:0xf bound_ctrl:1
	s_nop 0
	v_readlane_b32 s25, v38, 16
	v_readlane_b32 s35, v38, 48
	v_readlane_b32 s10, v38, 0
	v_readlane_b32 s11, v38, 32
	v_mov_b32_e32 v38, s25
	v_mov_b32_e32 v39, s35
	v_pk_add_f32 v[38:39], s[10:11], v[38:39]
	s_nop 0
	v_add_f32_e32 v38, v38, v39
	v_fmamk_f32 v38, v38, 0x3a800000, v1
	v_mul_f32_e32 v39, 0x4b800000, v38
	v_cmp_gt_f32_e32 vcc, s15, v38
	s_nop 1
	v_cndmask_b32_e32 v38, v38, v39, vcc
	v_rsq_f32_e32 v40, v38
	v_lshl_add_u64 v[38:39], s[58:59], 0, v[18:19]
	v_mul_f32_e32 v41, 0x45800000, v40
	v_cndmask_b32_e32 v40, v40, v41, vcc
	v_pk_mul_f32 v[22:23], v[22:23], v[40:41] op_sel_hi:[1,0]
	v_pk_mul_f32 v[24:25], v[24:25], v[40:41] op_sel_hi:[1,0]
	v_pk_mul_f32 v[26:27], v[26:27], v[40:41] op_sel_hi:[1,0]
	v_pk_mul_f32 v[28:29], v[28:29], v[40:41] op_sel_hi:[1,0]
	v_pk_mul_f32 v[34:35], v[34:35], v[40:41] op_sel_hi:[1,0]
	v_pk_mul_f32 v[36:37], v[36:37], v[40:41] op_sel_hi:[1,0]
	v_pk_mul_f32 v[30:31], v[30:31], v[40:41] op_sel_hi:[1,0]
	v_pk_mul_f32 v[32:33], v[32:33], v[40:41] op_sel_hi:[1,0]
	v_pk_mul_f32 v[24:25], v[4:5], v[24:25]
	v_pk_mul_f32 v[40:41], v[2:3], v[22:23]
	v_pk_mul_f32 v[28:29], v[8:9], v[28:29]
	v_pk_mul_f32 v[26:27], v[6:7], v[26:27]
	v_max_f32_e64 v22, |v40|, |v41|
	v_max_f32_e64 v23, |v24|, |v25|
	v_pk_mul_f32 v[36:37], v[12:13], v[36:37]
	v_pk_mul_f32 v[34:35], v[10:11], v[34:35]
	v_max_f32_e64 v44, |v26|, |v27|
	v_max_f32_e64 v45, |v28|, |v29|
	v_max3_f32 v22, v22, 0, v23
	v_pk_mul_f32 v[32:33], v[16:17], v[32:33]
	v_pk_mul_f32 v[30:31], v[14:15], v[30:31]
	v_max_f32_e64 v46, |v34|, |v35|
	v_max_f32_e64 v47, |v36|, |v37|
	v_max3_f32 v22, v22, v44, v45
	v_max_f32_e64 v48, |v30|, |v31|
	v_max_f32_e64 v50, |v32|, |v33|
	v_max3_f32 v22, v22, v46, v47
	v_max3_f32 v22, v22, v48, v50
	v_add_co_u32_e32 v38, vcc, s21, v38
	s_nop 0
	v_mov_b32_dpp v49, v22 row_ror:1 row_mask:0xf bank_mask:0xf
	v_max_f32_e32 v23, v49, v49
	v_max_f32_e32 v22, v22, v23
	v_addc_co_u32_e32 v39, vcc, 0, v39, vcc
	s_nop 0
	v_mov_b32_dpp v52, v22 row_ror:2 row_mask:0xf bank_mask:0xf
	v_max_f32_e32 v23, v52, v52
	v_max_f32_e32 v22, v22, v23
	s_nop 1
	v_mov_b32_dpp v42, v22 row_ror:4 row_mask:0xf bank_mask:0xf
	v_max_f32_e32 v23, v42, v42
	v_max_f32_e32 v22, v22, v23
	s_nop 1
	v_mov_b32_dpp v43, v22 row_ror:8 row_mask:0xf bank_mask:0xf
	v_max_f32_e32 v23, v43, v43
	v_max_f32_e32 v22, v22, v23
	s_nop 0
	v_readlane_b32 s25, v22, 32
	v_readlane_b32 s35, v22, 48
	v_readlane_b32 s10, v22, 0
	v_readlane_b32 s11, v22, 16
	v_max_f32_e64 v22, s35, s35
	v_max_f32_e64 v23, s25, s25
	v_mov_b32_e32 v42, s11
	v_max_f32_e32 v22, v23, v22
	v_max3_f32 v22, s10, v42, v22
	v_div_scale_f32 v23, s[10:11], v22, v22, s18
	v_rcp_f32_e32 v42, v23
	v_div_scale_f32 v43, vcc, s18, v22, s18
	v_fma_f32 v44, -v23, v42, 1.0
	v_fmac_f32_e32 v42, v44, v42
	v_mul_f32_e32 v44, v43, v42
	v_fma_f32 v45, -v23, v44, v43
	v_fmac_f32_e32 v44, v45, v42
	v_fma_f32 v23, -v23, v44, v43
	v_div_fmas_f32 v23, v23, v42, v44
	v_div_fixup_f32 v23, v23, v22, s18
	v_cmp_lt_f32_e32 vcc, 0, v22
	s_nop 1
	v_cndmask_b32_e32 v23, 0, v23, vcc
	v_fmaak_f32 v40, v40, v23, 0x4b400000
	v_fmaak_f32 v41, v41, v23, 0x4b400000
	v_fmaak_f32 v24, v24, v23, 0x4b400000
	v_fmaak_f32 v25, v25, v23, 0x4b400000
	v_fmaak_f32 v26, v26, v23, 0x4b400000
	v_fmaak_f32 v27, v27, v23, 0x4b400000
	v_fmaak_f32 v28, v28, v23, 0x4b400000
	v_fmaak_f32 v29, v29, v23, 0x4b400000
	v_perm_b32 v24, v25, v24, s19
	v_perm_b32 v25, v41, v40, s19
	v_fmaak_f32 v34, v34, v23, 0x4b400000
	v_fmaak_f32 v35, v35, v23, 0x4b400000
	v_fmaak_f32 v36, v36, v23, 0x4b400000
	v_fmaak_f32 v37, v37, v23, 0x4b400000
	v_perm_b32 v28, v29, v28, s19
	v_perm_b32 v26, v27, v26, s19
	v_perm_b32 v24, v24, v25, s20
	v_perm_b32 v27, v37, v36, s19
	v_perm_b32 v25, v28, v26, s20
	global_store_dword v[38:39], v24, off
	global_store_dword v[38:39], v25, off offset:256
	v_perm_b32 v24, v35, v34, s19
	v_perm_b32 v24, v27, v24, s20
	global_store_dword v[38:39], v24, off offset:512
	v_fmaak_f32 v24, v30, v23, 0x4b400000
	v_fmaak_f32 v25, v31, v23, 0x4b400000
	v_fmaak_f32 v26, v32, v23, 0x4b400000
	v_fmaak_f32 v23, v33, v23, 0x4b400000
	v_perm_b32 v23, v23, v26, s19
	v_perm_b32 v24, v25, v24, s19
	v_perm_b32 v23, v23, v24, s20
	global_store_dword v[38:39], v23, off offset:768
	s_and_saveexec_b64 s[10:11], s[2:3]
	s_cbranch_execz .LBB0_50
	s_add_u32 s44, s58, s12
	v_mul_f32_e32 v22, 0x3c010204, v22
	s_addc_u32 s45, s59, s13
	global_store_dword v165, v22, s[44:45]
	s_branch .LBB0_50

; #define GAS __attribute__((address_space(1)))
; #define LAS __attribute__((address_space(3)))
; #define LDS_WAIT() asm volatile("s_waitcnt lgkmcnt(0)" ::: "memory")
; __device__ __forceinline__ unsigned pk2(float lo, float hi) { return f2bf(lo) | (f2bf(hi) << 16); }
; __device__ __forceinline__ void p0_transpose_item(const float* W, int ldw, int csrc0, int k0, const float* gain, bf16* WT, int Kd, int drow0, LAS float* scr, int lane) {
;     { f32x4 v[8]; const int r8 = lane >> 3, c4 = (lane & 7) * 4;
; #pragma unroll
;       for (int i = 0; i < 8; ++i) v[i] = *(const GAS f32x4*)(W + (size_t)(k0 + 8 * i + r8) * ldw + csrc0 + c4);
; #pragma unroll
;       for (int i = 0; i < 8; ++i) { const int kk = 8 * i + r8; const float g = gain ? gain[k0 + kk] : 1.0f; scr[kk * 33 + c4] = v[i][0] * g; scr[kk * 33 + c4 + 1] = v[i][1] * g; scr[kk * 33 + c4 + 2] = v[i][2] * g; scr[kk * 33 + c4 + 3] = v[i][3] * g; } }
;     LDS_WAIT(); asm volatile("" ::: "memory");
;     const int c = lane & 7;
; #pragma unroll
;     for (int j = 0; j < 4; ++j) { const int n = (lane >> 3) + 8 * j; const LAS float* s = scr + (8 * c) * 33 + n;
;         u32x4 o; o.x = pk2(s[0 * 33], s[1 * 33]); o.y = pk2(s[2 * 33], s[3 * 33]); o.z = pk2(s[4 * 33], s[5 * 33]); o.w = pk2(s[6 * 33], s[7 * 33]);
;         *(GAS u32x4*)(WT + (size_t)(drow0 + n) * Kd + k0 + 8 * c) = o; }
;     LDS_WAIT(); asm volatile("" ::: "memory");
; }
; __device__ __forceinline__ void p0_prologue(Frame& F, const Args& A) {
;     ...
;     for (int r = gw; r < 2 * I_SQ; r += NGW) {
;         if (r < I_SQ) p0_transpose_item(A.in[10], D, (r % 32) * 32, (r / 32) * 64, nullptr, (bf16*)(ws + WS_WOUT), D, (r % 32) * 32, scr, lane);
;         else { const int q = r - I_SQ; p0_transpose_item(A.in[15], D, (q % 32) * 32, (q / 32) * 64, nullptr, (bf16*)(ws + WS_WXO), D, (q % 32) * 32, scr, lane); }
.LBB0_56:
	s_cmpk_gt_i32 s12, 0x1ff
	s_mov_b64 s[4:5], -1
	s_cbranch_scc0 .LBB0_58
	s_and_b32 s2, s8, 0x7fffffc0
	s_add_i32 s4, s2, 0xfffffc00
	s_and_b32 s13, s6, 0x3e0
	v_or_b32_e32 v2, s4, v167
	s_lshl_b32 s2, s13, 2
	v_or_b32_e32 v30, 8, v2
	v_mov_b32_e32 v31, v3
	v_or_b32_e32 v36, 16, v2
	v_mov_b32_e32 v37, v3
	v_or_b32_e32 v38, 24, v2
	v_mov_b32_e32 v39, v3
	v_or_b32_e32 v44, 32, v2
	v_mov_b32_e32 v45, v3
	v_or_b32_e32 v46, 40, v2
	v_mov_b32_e32 v47, v3
	v_lshl_add_u64 v[56:57], v[8:9], 0, s[2:3]
	v_lshlrev_b64 v[28:29], 12, v[2:3]
	v_lshlrev_b64 v[30:31], 12, v[30:31]
	v_lshlrev_b64 v[36:37], 12, v[36:37]
	v_lshlrev_b64 v[38:39], 12, v[38:39]
	v_lshlrev_b64 v[44:45], 12, v[44:45]
	v_lshlrev_b64 v[46:47], 12, v[46:47]
	v_lshl_add_u64 v[28:29], v[56:57], 0, v[28:29]
	v_lshl_add_u64 v[32:33], v[56:57], 0, v[30:31]
	v_lshl_add_u64 v[36:37], v[56:57], 0, v[36:37]
	v_lshl_add_u64 v[40:41], v[56:57], 0, v[38:39]
	v_lshl_add_u64 v[44:45], v[56:57], 0, v[44:45]
	v_lshl_add_u64 v[48:49], v[56:57], 0, v[46:47]
	global_load_dwordx4 v[28:31], v[28:29], off nt
	s_nop 0
	global_load_dwordx4 v[32:35], v[32:33], off nt
	s_nop 0
	global_load_dwordx4 v[36:39], v[36:37], off nt
	s_nop 0
	global_load_dwordx4 v[40:43], v[40:41], off nt
	s_nop 0
	global_load_dwordx4 v[44:47], v[44:45], off nt
	s_nop 0
	global_load_dwordx4 v[48:51], v[48:49], off nt
	v_or_b32_e32 v52, 48, v2
	v_mov_b32_e32 v53, v3
	v_lshlrev_b64 v[52:53], 12, v[52:53]
	v_lshl_add_u64 v[52:53], v[56:57], 0, v[52:53]
	v_or_b32_e32 v2, 56, v2
	global_load_dwordx4 v[52:55], v[52:53], off nt
	v_lshlrev_b64 v[58:59], 12, v[2:3]
	v_lshl_add_u64 v[56:57], v[56:57], 0, v[58:59]
	global_load_dwordx4 v[56:59], v[56:57], off nt
	s_mov_b32 s5, s3
	v_or_b32_e32 v2, s13, v167
	v_lshl_add_u64 v[60:61], s[4:5], 1, v[4:5]
	v_lshlrev_b32_e32 v2, 11, v2
	v_lshl_add_u64 v[62:63], v[60:61], 0, v[2:3]
	s_mov_b64 s[4:5], 0
	s_waitcnt vmcnt(7)
	ds_write2_b32 v12, v28, v29 offset1:1
	ds_write2_b32 v12, v30, v31 offset0:2 offset1:3
	s_waitcnt vmcnt(6)
	ds_write2_b32 v13, v32, v33 offset1:1
	ds_write2_b32 v14, v34, v35 offset1:1
	s_waitcnt vmcnt(5)
	ds_write2_b32 v15, v36, v37 offset1:1
	ds_write2_b32 v16, v38, v39 offset1:1
	s_waitcnt vmcnt(4)
	ds_write2_b32 v17, v40, v41 offset1:1
	ds_write2_b32 v18, v42, v43 offset1:1
	s_waitcnt vmcnt(3)
	ds_write2_b32 v19, v44, v45 offset1:1
	ds_write2_b32 v20, v46, v47 offset1:1
	s_waitcnt vmcnt(2)
	ds_write2_b32 v21, v48, v49 offset1:1
	ds_write2_b32 v22, v50, v51 offset1:1
	s_waitcnt vmcnt(1)
	ds_write2_b32 v23, v52, v53 offset1:1
	ds_write2_b32 v24, v54, v55 offset1:1
	s_waitcnt vmcnt(0)
	ds_write2_b32 v25, v56, v57 offset1:1
	ds_write2_b32 v26, v58, v59 offset1:1
	s_waitcnt lgkmcnt(0)
	ds_read2_b32 v[32:33], v1 offset0:33 offset1:41
	ds_read2_b32 v[34:35], v1 offset1:8
	ds_read2_b32 v[36:37], v1 offset0:66 offset1:74
	ds_read2_b32 v[38:39], v1 offset0:99 offset1:107
	ds_read2_b32 v[40:41], v1 offset0:132 offset1:140
	ds_read2_b32 v[42:43], v1 offset0:165 offset1:173
	ds_read2_b32 v[44:45], v1 offset0:198 offset1:206
	ds_read2_b32 v[46:47], v1 offset0:231 offset1:239
	s_waitcnt lgkmcnt(6)
	v_bfe_u32 v2, v34, 16, 1
	v_bfe_u32 v27, v32, 16, 1
	s_waitcnt lgkmcnt(5)
	v_bfe_u32 v28, v36, 16, 1
	v_add3_u32 v2, v34, v2, s10
	s_waitcnt lgkmcnt(3)
	v_bfe_u32 v30, v40, 16, 1
	s_waitcnt lgkmcnt(1)
	v_bfe_u32 v48, v44, 16, 1
	v_add3_u32 v27, v32, v27, s10
	v_add3_u32 v28, v36, v28, s10
	v_lshrrev_b32_e32 v2, 16, v2
	v_bfe_u32 v29, v38, 16, 1
	v_bfe_u32 v31, v42, 16, 1
	s_waitcnt lgkmcnt(0)
	v_bfe_u32 v49, v46, 16, 1
	v_add3_u32 v30, v40, v30, s10
	v_add3_u32 v32, v44, v48, s10
	v_lshrrev_b32_e32 v36, 16, v28
	v_and_or_b32 v28, v27, s11, v2
	v_bfe_u32 v2, v35, 16, 1
	v_add3_u32 v29, v38, v29, s10
	v_add3_u32 v31, v42, v31, s10
	v_add3_u32 v34, v46, v49, s10
	v_lshrrev_b32_e32 v30, 16, v30
	v_lshrrev_b32_e32 v32, 16, v32
	v_add3_u32 v2, v35, v2, s10
	v_bfe_u32 v27, v33, 16, 1
	v_and_or_b32 v29, v29, s11, v36
	v_and_or_b32 v30, v31, s11, v30
	v_and_or_b32 v31, v34, s11, v32
	v_lshrrev_b32_e32 v2, 16, v2
	v_add3_u32 v27, v33, v27, s10
	global_store_dwordx4 v[62:63], v[28:31], off
	ds_read2_b32 v[32:33], v1 offset0:16 offset1:24
	s_nop 0
	v_and_or_b32 v28, v27, s11, v2
	v_bfe_u32 v2, v37, 16, 1
	v_add3_u32 v2, v37, v2, s10
	v_bfe_u32 v27, v39, 16, 1
	v_lshrrev_b32_e32 v2, 16, v2
	v_add3_u32 v27, v39, v27, s10
	v_and_or_b32 v29, v27, s11, v2
	v_bfe_u32 v2, v41, 16, 1
	v_add3_u32 v2, v41, v2, s10
	v_bfe_u32 v27, v43, 16, 1
	v_lshrrev_b32_e32 v2, 16, v2
	v_add3_u32 v27, v43, v27, s10
	v_and_or_b32 v30, v27, s11, v2
	v_bfe_u32 v2, v45, 16, 1
	v_add3_u32 v2, v45, v2, s10
	v_bfe_u32 v27, v47, 16, 1
	v_lshrrev_b32_e32 v2, 16, v2
	v_add3_u32 v27, v47, v27, s10
	v_and_or_b32 v31, v27, s11, v2
	v_or_b32_e32 v2, s13, v81
	v_lshlrev_b32_e32 v2, 11, v2
	v_lshl_add_u64 v[34:35], v[60:61], 0, v[2:3]
	global_store_dwordx4 v[34:35], v[28:31], off
	ds_read2_b32 v[34:35], v1 offset0:49 offset1:57
	ds_read2_b32 v[36:37], v1 offset0:82 offset1:90
	ds_read2_b32 v[38:39], v1 offset0:115 offset1:123
	s_waitcnt lgkmcnt(3)
	v_bfe_u32 v2, v32, 16, 1
	v_add3_u32 v2, v32, v2, s10
	s_waitcnt lgkmcnt(2)
	v_bfe_u32 v27, v34, 16, 1
	ds_read2_b32 v[40:41], v1 offset0:148 offset1:156
	v_lshrrev_b32_e32 v2, 16, v2
	v_add3_u32 v27, v34, v27, s10
	ds_read2_b32 v[42:43], v1 offset0:181 offset1:189
	v_and_or_b32 v28, v27, s11, v2
	s_waitcnt lgkmcnt(3)
	v_bfe_u32 v2, v36, 16, 1
	v_add3_u32 v2, v36, v2, s10
	s_waitcnt lgkmcnt(2)
	v_bfe_u32 v27, v38, 16, 1
	ds_read2_b32 v[44:45], v1 offset0:214 offset1:222
	v_lshrrev_b32_e32 v2, 16, v2
	v_add3_u32 v27, v38, v27, s10
	ds_read2_b32 v[46:47], v1 offset0:247 offset1:255
	v_and_or_b32 v29, v27, s11, v2
	s_waitcnt lgkmcnt(3)
; #define GAS __attribute__((address_space(1)))
; #define LAS __attribute__((address_space(3)))
; #define LDS_WAIT() asm volatile("s_waitcnt lgkmcnt(0)" ::: "memory")
; __device__ __forceinline__ unsigned pk2(float lo, float hi) { return f2bf(lo) | (f2bf(hi) << 16); }
; __device__ __forceinline__ void p0_transpose_item(const float* W, int ldw, int csrc0, int k0, const float* gain, bf16* WT, int Kd, int drow0, LAS float* scr, int lane) {
;     { f32x4 v[8]; const int r8 = lane >> 3, c4 = (lane & 7) * 4;
; #pragma unroll
;       for (int i = 0; i < 8; ++i) v[i] = *(const GAS f32x4*)(W + (size_t)(k0 + 8 * i + r8) * ldw + csrc0 + c4);
; #pragma unroll
;       for (int i = 0; i < 8; ++i) { const int kk = 8 * i + r8; const float g = gain ? gain[k0 + kk] : 1.0f; scr[kk * 33 + c4] = v[i][0] * g; scr[kk * 33 + c4 + 1] = v[i][1] * g; scr[kk * 33 + c4 + 2] = v[i][2] * g; scr[kk * 33 + c4 + 3] = v[i][3] * g; } }
;     LDS_WAIT(); asm volatile("" ::: "memory");
;     const int c = lane & 7;
; #pragma unroll
;     for (int j = 0; j < 4; ++j) { const int n = (lane >> 3) + 8 * j; const LAS float* s = scr + (8 * c) * 33 + n;
;         u32x4 o; o.x = pk2(s[0 * 33], s[1 * 33]); o.y = pk2(s[2 * 33], s[3 * 33]); o.z = pk2(s[4 * 33], s[5 * 33]); o.w = pk2(s[6 * 33], s[7 * 33]);
;         *(GAS u32x4*)(WT + (size_t)(drow0 + n) * Kd + k0 + 8 * c) = o; }
;     LDS_WAIT(); asm volatile("" ::: "memory");
; }
; __device__ __forceinline__ void p0_prologue(Frame& F, const Args& A) {
;     ...
;         if (r < I_SQ) p0_transpose_item(A.in[10], D, (r % 32) * 32, (r / 32) * 64, nullptr, (bf16*)(ws + WS_WOUT), D, (r % 32) * 32, scr, lane);
	v_bfe_u32 v2, v40, 16, 1
	v_add3_u32 v2, v40, v2, s10
	s_waitcnt lgkmcnt(2)
	v_bfe_u32 v27, v42, 16, 1
	v_lshrrev_b32_e32 v2, 16, v2
	v_add3_u32 v27, v42, v27, s10
	v_and_or_b32 v30, v27, s11, v2
	s_waitcnt lgkmcnt(1)
	v_bfe_u32 v2, v44, 16, 1
	v_add3_u32 v2, v44, v2, s10
	s_waitcnt lgkmcnt(0)
	v_bfe_u32 v27, v46, 16, 1
	v_lshrrev_b32_e32 v2, 16, v2
	v_add3_u32 v27, v46, v27, s10
	v_and_or_b32 v31, v27, s11, v2
	v_or_b32_e32 v2, s13, v82
	v_lshlrev_b32_e32 v2, 11, v2
	v_lshl_add_u64 v[48:49], v[60:61], 0, v[2:3]
	v_bfe_u32 v2, v33, 16, 1
	v_add3_u32 v2, v33, v2, s10
	v_bfe_u32 v27, v35, 16, 1
	v_lshrrev_b32_e32 v2, 16, v2
	v_add3_u32 v27, v35, v27, s10
	global_store_dwordx4 v[48:49], v[28:31], off
	s_nop 1
	v_and_or_b32 v28, v27, s11, v2
	v_bfe_u32 v2, v37, 16, 1
	v_add3_u32 v2, v37, v2, s10
	v_bfe_u32 v27, v39, 16, 1
	v_lshrrev_b32_e32 v2, 16, v2
	v_add3_u32 v27, v39, v27, s10
	v_and_or_b32 v29, v27, s11, v2
	v_bfe_u32 v2, v41, 16, 1
	v_add3_u32 v2, v41, v2, s10
	v_bfe_u32 v27, v43, 16, 1
	v_lshrrev_b32_e32 v2, 16, v2
	v_add3_u32 v27, v43, v27, s10
	v_and_or_b32 v30, v27, s11, v2
	v_bfe_u32 v2, v45, 16, 1
	v_add3_u32 v2, v45, v2, s10
	v_bfe_u32 v27, v47, 16, 1
	v_lshrrev_b32_e32 v2, 16, v2
	v_add3_u32 v27, v47, v27, s10
	v_and_or_b32 v31, v27, s11, v2
	v_or_b32_e32 v2, s13, v83
	v_lshlrev_b32_e32 v2, 11, v2
	v_lshl_add_u64 v[32:33], v[60:61], 0, v[2:3]
	global_store_dwordx4 v[32:33], v[28:31], off
	s_waitcnt lgkmcnt(0)
.LBB0_58:
	s_andn2_b64 vcc, exec, s[4:5]
	s_cbranch_vccnz .LBB0_55
	s_ashr_i32 s2, s12, 31
	s_lshr_b32 s2, s2, 27
	s_add_i32 s2, s12, s2
	s_ashr_i32 s2, s2, 5
	s_lshl_b32 s18, s2, 6
	s_lshl_b32 s4, s2, 10
	v_or_b32_e32 v56, s18, v167
	s_sub_i32 s4, s6, s4
	v_or_b32_e32 v30, 8, v56
	v_or_b32_e32 v36, 16, v56
	v_or_b32_e32 v38, 24, v56
	v_or_b32_e32 v44, 32, v56
	v_or_b32_e32 v46, 40, v56
	s_ashr_i32 s5, s4, 31
	v_ashrrev_i32_e32 v57, 31, v56
	v_ashrrev_i32_e32 v31, 31, v30
	v_ashrrev_i32_e32 v37, 31, v36
	v_ashrrev_i32_e32 v39, 31, v38
	v_ashrrev_i32_e32 v45, 31, v44
	v_ashrrev_i32_e32 v47, 31, v46
	v_lshl_add_u64 v[58:59], s[4:5], 2, v[10:11]
	v_lshlrev_b64 v[28:29], 12, v[56:57]
	v_lshlrev_b64 v[30:31], 12, v[30:31]
	v_lshlrev_b64 v[36:37], 12, v[36:37]
	v_lshlrev_b64 v[38:39], 12, v[38:39]
	v_lshlrev_b64 v[44:45], 12, v[44:45]
	v_lshlrev_b64 v[46:47], 12, v[46:47]
	v_lshl_add_u64 v[28:29], v[58:59], 0, v[28:29]
	v_lshl_add_u64 v[32:33], v[58:59], 0, v[30:31]
	v_lshl_add_u64 v[36:37], v[58:59], 0, v[36:37]
	v_lshl_add_u64 v[40:41], v[58:59], 0, v[38:39]
	v_lshl_add_u64 v[44:45], v[58:59], 0, v[44:45]
	v_lshl_add_u64 v[48:49], v[58:59], 0, v[46:47]
	global_load_dwordx4 v[28:31], v[28:29], off nt
	s_nop 0
	global_load_dwordx4 v[32:35], v[32:33], off nt
	s_nop 0
	global_load_dwordx4 v[36:39], v[36:37], off nt
	s_nop 0
	global_load_dwordx4 v[40:43], v[40:41], off nt
	s_nop 0
	global_load_dwordx4 v[44:47], v[44:45], off nt
	s_nop 0
	global_load_dwordx4 v[48:51], v[48:49], off nt
	v_or_b32_e32 v52, 48, v56
	v_ashrrev_i32_e32 v53, 31, v52
	v_lshlrev_b64 v[52:53], 12, v[52:53]
	v_or_b32_e32 v56, 56, v56
	v_lshl_add_u64 v[52:53], v[58:59], 0, v[52:53]
	v_ashrrev_i32_e32 v57, 31, v56
	global_load_dwordx4 v[52:55], v[52:53], off nt
	v_lshlrev_b64 v[56:57], 12, v[56:57]
	v_lshl_add_u64 v[56:57], v[58:59], 0, v[56:57]
	global_load_dwordx4 v[56:59], v[56:57], off nt
	v_add_u32_e32 v62, s4, v167
	s_ashr_i32 s19, s18, 31
	v_ashrrev_i32_e32 v63, 31, v62
	v_lshl_add_u64 v[60:61], s[18:19], 1, v[6:7]
	s_waitcnt vmcnt(7)
	ds_write2_b32 v12, v28, v29 offset1:1
	ds_write2_b32 v12, v30, v31 offset0:2 offset1:3
	s_waitcnt vmcnt(6)
	ds_write2_b32 v13, v32, v33 offset1:1
	ds_write2_b32 v14, v34, v35 offset1:1
	s_waitcnt vmcnt(5)
	ds_write2_b32 v15, v36, v37 offset1:1
	ds_write2_b32 v16, v38, v39 offset1:1
	s_waitcnt vmcnt(4)
	ds_write2_b32 v17, v40, v41 offset1:1
	ds_write2_b32 v18, v42, v43 offset1:1
	s_waitcnt vmcnt(3)
	ds_write2_b32 v19, v44, v45 offset1:1
	ds_write2_b32 v20, v46, v47 offset1:1
	s_waitcnt vmcnt(2)
	ds_write2_b32 v21, v48, v49 offset1:1
	ds_write2_b32 v22, v50, v51 offset1:1
	s_waitcnt vmcnt(1)
	ds_write2_b32 v23, v52, v53 offset1:1
	ds_write2_b32 v24, v54, v55 offset1:1
	s_waitcnt vmcnt(0)
	ds_write2_b32 v25, v56, v57 offset1:1
	ds_write2_b32 v26, v58, v59 offset1:1
	s_waitcnt lgkmcnt(0)
	ds_read2_b32 v[32:33], v1 offset0:33 offset1:41
	ds_read2_b32 v[34:35], v1 offset1:8
	ds_read2_b32 v[36:37], v1 offset0:66 offset1:74
	ds_read2_b32 v[38:39], v1 offset0:99 offset1:107
	ds_read2_b32 v[40:41], v1 offset0:132 offset1:140
	ds_read2_b32 v[42:43], v1 offset0:165 offset1:173
	ds_read2_b32 v[44:45], v1 offset0:198 offset1:206
	ds_read2_b32 v[46:47], v1 offset0:231 offset1:239
	s_waitcnt lgkmcnt(6)
	v_bfe_u32 v2, v34, 16, 1
	v_bfe_u32 v27, v32, 16, 1
	s_waitcnt lgkmcnt(5)
	v_bfe_u32 v28, v36, 16, 1
	v_add3_u32 v2, v34, v2, s10
	s_waitcnt lgkmcnt(3)
	v_bfe_u32 v30, v40, 16, 1
	s_waitcnt lgkmcnt(1)
	v_bfe_u32 v48, v44, 16, 1
	v_add3_u32 v27, v32, v27, s10
	v_add3_u32 v28, v36, v28, s10
	v_lshrrev_b32_e32 v2, 16, v2
	v_bfe_u32 v29, v38, 16, 1
	v_bfe_u32 v31, v42, 16, 1
	s_waitcnt lgkmcnt(0)
; #define GAS __attribute__((address_space(1)))
; #define LAS __attribute__((address_space(3)))
; #define LDS_WAIT() asm volatile("s_waitcnt lgkmcnt(0)" ::: "memory")
; __device__ __forceinline__ unsigned pk2(float lo, float hi) { return f2bf(lo) | (f2bf(hi) << 16); }
; __device__ __forceinline__ void p0_transpose_item(const float* W, int ldw, int csrc0, int k0, const float* gain, bf16* WT, int Kd, int drow0, LAS float* scr, int lane) {
;     { f32x4 v[8]; const int r8 = lane >> 3, c4 = (lane & 7) * 4;
; #pragma unroll
;       for (int i = 0; i < 8; ++i) v[i] = *(const GAS f32x4*)(W + (size_t)(k0 + 8 * i + r8) * ldw + csrc0 + c4);
; #pragma unroll
;       for (int i = 0; i < 8; ++i) { const int kk = 8 * i + r8; const float g = gain ? gain[k0 + kk] : 1.0f; scr[kk * 33 + c4] = v[i][0] * g; scr[kk * 33 + c4 + 1] = v[i][1] * g; scr[kk * 33 + c4 + 2] = v[i][2] * g; scr[kk * 33 + c4 + 3] = v[i][3] * g; } }
;     LDS_WAIT(); asm volatile("" ::: "memory");
;     const int c = lane & 7;
; #pragma unroll
;     for (int j = 0; j < 4; ++j) { const int n = (lane >> 3) + 8 * j; const LAS float* s = scr + (8 * c) * 33 + n;
;         u32x4 o; o.x = pk2(s[0 * 33], s[1 * 33]); o.y = pk2(s[2 * 33], s[3 * 33]); o.z = pk2(s[4 * 33], s[5 * 33]); o.w = pk2(s[6 * 33], s[7 * 33]);
;         *(GAS u32x4*)(WT + (size_t)(drow0 + n) * Kd + k0 + 8 * c) = o; }
;     LDS_WAIT(); asm volatile("" ::: "memory");
; }
	v_bfe_u32 v49, v46, 16, 1
	v_add3_u32 v30, v40, v30, s10
	v_add3_u32 v32, v44, v48, s10
	v_lshrrev_b32_e32 v36, 16, v28
	v_and_or_b32 v28, v27, s11, v2
	v_bfe_u32 v2, v35, 16, 1
	v_add3_u32 v29, v38, v29, s10
	v_add3_u32 v31, v42, v31, s10
	v_add3_u32 v34, v46, v49, s10
	v_lshrrev_b32_e32 v30, 16, v30
	v_lshrrev_b32_e32 v32, 16, v32
	v_lshlrev_b64 v[48:49], 11, v[62:63]
	v_add3_u32 v2, v35, v2, s10
	v_bfe_u32 v27, v33, 16, 1
	v_and_or_b32 v29, v29, s11, v36
	v_and_or_b32 v30, v31, s11, v30
	v_and_or_b32 v31, v34, s11, v32
	v_lshl_add_u64 v[48:49], v[60:61], 0, v[48:49]
	v_lshrrev_b32_e32 v2, 16, v2
	v_add3_u32 v27, v33, v27, s10
	global_store_dwordx4 v[48:49], v[28:31], off
	v_add_u32_e32 v32, 8, v62
	v_ashrrev_i32_e32 v33, 31, v32
	v_and_or_b32 v28, v27, s11, v2
	v_bfe_u32 v2, v37, 16, 1
	v_add3_u32 v2, v37, v2, s10
	v_bfe_u32 v27, v39, 16, 1
	v_lshrrev_b32_e32 v2, 16, v2
	v_add3_u32 v27, v39, v27, s10
	v_and_or_b32 v29, v27, s11, v2
	v_bfe_u32 v2, v41, 16, 1
	v_add3_u32 v2, v41, v2, s10
	v_bfe_u32 v27, v43, 16, 1
	v_lshrrev_b32_e32 v2, 16, v2
	v_add3_u32 v27, v43, v27, s10
	v_and_or_b32 v30, v27, s11, v2
	v_bfe_u32 v2, v45, 16, 1
	v_add3_u32 v2, v45, v2, s10
	v_bfe_u32 v27, v47, 16, 1
	v_lshrrev_b32_e32 v2, 16, v2
	v_add3_u32 v27, v47, v27, s10
	v_lshlrev_b64 v[32:33], 11, v[32:33]
	v_and_or_b32 v31, v27, s11, v2
	ds_read2_b32 v[34:35], v1 offset0:16 offset1:24
	v_lshl_add_u64 v[32:33], v[60:61], 0, v[32:33]
	global_store_dwordx4 v[32:33], v[28:31], off
	ds_read2_b32 v[32:33], v1 offset0:49 offset1:57
	ds_read2_b32 v[36:37], v1 offset0:82 offset1:90
	ds_read2_b32 v[38:39], v1 offset0:115 offset1:123
	s_waitcnt lgkmcnt(3)
	v_bfe_u32 v2, v34, 16, 1
	v_add3_u32 v2, v34, v2, s10
	s_waitcnt lgkmcnt(2)
	v_bfe_u32 v27, v32, 16, 1
	ds_read2_b32 v[40:41], v1 offset0:148 offset1:156
	v_lshrrev_b32_e32 v2, 16, v2
	v_add3_u32 v27, v32, v27, s10
	ds_read2_b32 v[42:43], v1 offset0:181 offset1:189
	v_and_or_b32 v28, v27, s11, v2
	s_waitcnt lgkmcnt(3)
	v_bfe_u32 v2, v36, 16, 1
	v_add3_u32 v2, v36, v2, s10
	s_waitcnt lgkmcnt(2)
	v_bfe_u32 v27, v38, 16, 1
	ds_read2_b32 v[44:45], v1 offset0:214 offset1:222
	v_lshrrev_b32_e32 v2, 16, v2
	v_add3_u32 v27, v38, v27, s10
	ds_read2_b32 v[46:47], v1 offset0:247 offset1:255
	v_and_or_b32 v29, v27, s11, v2
	s_waitcnt lgkmcnt(3)
	v_bfe_u32 v2, v40, 16, 1
	v_add3_u32 v2, v40, v2, s10
	s_waitcnt lgkmcnt(2)
	v_bfe_u32 v27, v42, 16, 1
	v_lshrrev_b32_e32 v2, 16, v2
	v_add3_u32 v27, v42, v27, s10
	v_and_or_b32 v30, v27, s11, v2
	s_waitcnt lgkmcnt(1)
	v_bfe_u32 v2, v44, 16, 1
	v_add3_u32 v2, v44, v2, s10
	s_waitcnt lgkmcnt(0)
	v_bfe_u32 v27, v46, 16, 1
	v_lshrrev_b32_e32 v2, 16, v2
	v_add3_u32 v27, v46, v27, s10
	v_add_u32_e32 v48, 16, v62
	v_and_or_b32 v31, v27, s11, v2
	v_ashrrev_i32_e32 v49, 31, v48
	v_bfe_u32 v2, v35, 16, 1
	v_lshlrev_b64 v[48:49], 11, v[48:49]
	v_add3_u32 v2, v35, v2, s10
	v_bfe_u32 v27, v33, 16, 1
	v_lshl_add_u64 v[48:49], v[60:61], 0, v[48:49]
	v_lshrrev_b32_e32 v2, 16, v2
	v_add3_u32 v27, v33, v27, s10
	global_store_dwordx4 v[48:49], v[28:31], off
	v_add_u32_e32 v32, 24, v62
	v_ashrrev_i32_e32 v33, 31, v32
	v_and_or_b32 v28, v27, s11, v2
	v_bfe_u32 v2, v37, 16, 1
	v_add3_u32 v2, v37, v2, s10
	v_bfe_u32 v27, v39, 16, 1
	v_lshrrev_b32_e32 v2, 16, v2
	v_add3_u32 v27, v39, v27, s10
	v_and_or_b32 v29, v27, s11, v2
	v_bfe_u32 v2, v41, 16, 1
	v_add3_u32 v2, v41, v2, s10
	v_bfe_u32 v27, v43, 16, 1
	v_lshrrev_b32_e32 v2, 16, v2
	v_add3_u32 v27, v43, v27, s10
	v_and_or_b32 v30, v27, s11, v2
	v_bfe_u32 v2, v45, 16, 1
	v_add3_u32 v2, v45, v2, s10
	v_bfe_u32 v27, v47, 16, 1
	v_lshrrev_b32_e32 v2, 16, v2
	v_add3_u32 v27, v47, v27, s10
	v_lshlrev_b64 v[32:33], 11, v[32:33]
	v_and_or_b32 v31, v27, s11, v2
	v_lshl_add_u64 v[32:33], v[60:61], 0, v[32:33]
	global_store_dwordx4 v[32:33], v[28:31], off
	s_waitcnt lgkmcnt(0)
	s_branch .LBB0_55
.LBB0_60:
	v_lshlrev_b32_e32 v2, 2, v198
	v_and_b32_e32 v34, 0x7c, v2
	s_cmpk_lt_i32 s33, 0x1800
	v_lshrrev_b32_e32 v1, 5, v196
	v_mov_b32_e32 v69, 0
	v_lshlrev_b32_e32 v70, 2, v34
	s_barrier
	s_cbranch_scc0 .LBB0_62
	s_ashr_i32 s2, s33, 31
	s_lshr_b32 s2, s2, 21
	s_add_i32 s2, s33, s2
	s_and_b32 s2, s2, 0xfffff800
	s_sub_i32 s2, s33, s2
	s_ashr_i32 s2, s2, 6
	s_ashr_i32 s3, s2, 31
	s_and_b32 s5, s33, 56
	s_and_b32 s4, s33, 0xfffff800
	s_lshl_b64 s[2:3], s[2:3], 22
	s_add_i32 s5, s93, s5
	s_cmpk_eq_i32 s4, 0x800
	s_cselect_b32 s6, s86, s82
	s_cselect_b32 s7, s87, s83
	s_cmpk_eq_i32 s4, 0x1000
	s_cselect_b32 s6, s90, s6
	s_cselect_b32 s4, s91, s7
	s_add_u32 s2, s6, s2
	v_lshl_or_b32 v68, s5, 4, v1
	s_addc_u32 s3, s4, s3
	v_lshlrev_b64 v[2:3], 12, v[68:69]
	v_lshl_add_u64 v[2:3], s[2:3], 0, v[2:3]
	s_lshl_b32 s2, s33, 9
	s_mov_b32 s5, 0
	s_and_b32 s4, s2, 0xe00
	v_lshl_add_u64 v[2:3], v[2:3], 0, s[4:5]
	v_mov_b32_e32 v71, v69
	v_lshl_add_u64 v[26:27], v[2:3], 0, v[70:71]
	s_movk_i32 s2, 0x2000
	v_add_co_u32_e32 v6, vcc, s2, v26
	s_movk_i32 s2, 0x4000
	s_nop 0
	v_addc_co_u32_e32 v7, vcc, 0, v27, vcc
	v_add_co_u32_e32 v10, vcc, s2, v26
	s_movk_i32 s2, 0x6000
	s_nop 0
	v_addc_co_u32_e32 v11, vcc, 0, v27, vcc
	v_add_co_u32_e32 v14, vcc, s2, v26
	s_mov_b32 s2, 0x8000
	s_nop 0
	v_addc_co_u32_e32 v15, vcc, 0, v27, vcc
	v_add_co_u32_e32 v18, vcc, s2, v26
	s_mov_b32 s2, 0xa000
	s_nop 0
	v_addc_co_u32_e32 v19, vcc, 0, v27, vcc
	v_add_co_u32_e32 v22, vcc, s2, v26
	global_load_dwordx4 v[2:5], v[26:27], off nt
	s_nop 0
	global_load_dwordx4 v[6:9], v[6:7], off nt
	v_addc_co_u32_e32 v23, vcc, 0, v27, vcc
	v_add_co_u32_e32 v28, vcc, 0xc000, v26
	global_load_dwordx4 v[10:13], v[10:11], off nt
	s_nop 0
	global_load_dwordx4 v[14:17], v[14:15], off nt
	v_addc_co_u32_e32 v29, vcc, 0, v27, vcc
	v_add_co_u32_e32 v30, vcc, 0xe000, v26
	global_load_dwordx4 v[18:21], v[18:19], off nt
	s_nop 0
	global_load_dwordx4 v[22:25], v[22:23], off nt
	v_addc_co_u32_e32 v31, vcc, 0, v27, vcc
	global_load_dwordx4 v[26:29], v[28:29], off nt
	s_nop 0
	global_load_dwordx4 v[30:33], v[30:31], off nt

; __device__ __forceinline__ void p0_prologue(Frame& F, const Args& A) {
;     ...
; #pragma unroll 1
;             while (r < NT2) {
;                 int rn = r + F.G; if (rn < NT2) P0T_ISSUE(rn, vb);
;                 P0T_PROCESS(r, va); r = rn; if (r >= NT2) break;
;                 rn = r + F.G; if (rn < NT2) P0T_ISSUE(rn, va);
;                 P0T_PROCESS(r, vb); r = rn; }
.LBB0_65:
	s_cmpk_gt_i32 s40, 0x17ff
	s_mov_b64 s[8:9], -1
	s_cbranch_scc1 .LBB0_64
	s_add_i32 s41, s40, s92
	s_cmpk_lt_i32 s41, 0x1800
	s_cselect_b64 s[10:11], -1, 0
	s_cmpk_gt_i32 s41, 0x17ff
	s_cselect_b64 s[8:9], -1, 0
	s_and_b64 vcc, exec, s[8:9]
	s_cbranch_vccnz .LBB0_68
	s_ashr_i32 s2, s41, 31
	s_lshr_b32 s2, s2, 21
	s_add_i32 s2, s41, s2
	s_and_b32 s2, s2, 0xfffff800
	s_sub_i32 s2, s41, s2
	s_ashr_i32 s2, s2, 6
	s_and_b32 s3, s41, 0xfffff800
	s_cmpk_eq_i32 s3, 0x800
	s_cselect_b32 s4, s86, s82
	s_cselect_b32 s12, s87, s83
	s_cmpk_eq_i32 s3, 0x1000
	s_cselect_b32 s12, s91, s12
	s_cselect_b32 s4, s90, s4
	s_ashr_i32 s3, s2, 31
	s_lshl_b64 s[2:3], s[2:3], 22
	s_add_u32 s2, s4, s2
	s_addc_u32 s3, s12, s3
	s_and_b32 s4, s41, 56
	s_add_i32 s4, s4, s93
	v_lshl_or_b32 v68, s4, 4, v1
	v_lshlrev_b64 v[34:35], 12, v[68:69]
	v_lshl_add_u64 v[34:35], s[2:3], 0, v[34:35]
	s_lshl_b32 s2, s41, 9
	s_and_b32 s4, s2, 0xe00
	v_lshl_add_u64 v[34:35], v[34:35], 0, s[4:5]
	v_mov_b32_e32 v71, v69
	v_lshl_add_u64 v[58:59], v[34:35], 0, v[70:71]
	v_add_co_u32_e32 v38, vcc, s21, v58
	s_nop 1
	v_addc_co_u32_e32 v39, vcc, 0, v59, vcc
	v_add_co_u32_e32 v42, vcc, s24, v58
	global_load_dwordx4 v[34:37], v[58:59], off nt
	s_nop 0
	global_load_dwordx4 v[38:41], v[38:39], off nt
	v_addc_co_u32_e32 v43, vcc, 0, v59, vcc
	v_add_co_u32_e32 v46, vcc, s25, v58
	s_nop 1
	v_addc_co_u32_e32 v47, vcc, 0, v59, vcc
	v_add_co_u32_e32 v50, vcc, s35, v58
	global_load_dwordx4 v[42:45], v[42:43], off nt
	s_nop 0
	global_load_dwordx4 v[46:49], v[46:47], off nt
	v_addc_co_u32_e32 v51, vcc, 0, v59, vcc
	v_add_co_u32_e32 v54, vcc, 0xa000, v58
	s_nop 1
	v_addc_co_u32_e32 v55, vcc, 0, v59, vcc
	v_add_co_u32_e32 v60, vcc, 0xc000, v58
	global_load_dwordx4 v[50:53], v[50:51], off nt
	s_nop 0
	global_load_dwordx4 v[54:57], v[54:55], off nt
	v_addc_co_u32_e32 v61, vcc, 0, v59, vcc
	v_add_co_u32_e32 v62, vcc, 0xe000, v58
	s_nop 1
	v_addc_co_u32_e32 v63, vcc, 0, v59, vcc
	global_load_dwordx4 v[58:61], v[60:61], off nt
	s_nop 0
	global_load_dwordx4 v[62:65], v[62:63], off nt

; __device__ __forceinline__ void p0_prologue(Frame& F, const Args& A) {
;     ...
;                 rn = r + F.G; if (rn < NT2) P0T_ISSUE(rn, va);
.LBB0_84:
	s_ashr_i32 s2, s40, 31
	s_lshr_b32 s2, s2, 21
	s_add_i32 s2, s40, s2
	s_ashr_i32 s44, s2, 11
	s_and_b32 s2, s2, 0xfffff800
	s_lshl_b32 s3, s40, 7
	s_sub_i32 s2, s40, s2
	s_and_b32 s3, s3, 0x380
	s_waitcnt vmcnt(0)
	v_pk_mul_f32 v[98:99], v[30:31], v[80:81] op_sel_hi:[1,0]
	v_add_u32_e32 v105, 0x1428, v92
	s_ashr_i32 s2, s2, 6
	s_add_i32 s40, s3, s7
	ds_write2_b32 v105, v98, v99 offset1:1
	v_pk_mul_f32 v[98:99], v[32:33], v[80:81] op_sel_hi:[1,0]
	v_add_u32_e32 v106, 0x1430, v92
	s_ashr_i32 s3, s2, 31
	s_lshl_b32 s45, s40, 1
	s_lshl_b32 s44, s44, 3
	ds_write2_b32 v106, v98, v99 offset1:1
	s_lshl_b64 s[18:19], s[2:3], 11
	s_and_b32 s45, s45, 0x7fffff00
	s_ashr_i32 s50, s44, 31
	v_add_u32_e32 v98, 0x400, v86
	v_add_u32_e32 v99, 0x800, v86
	s_waitcnt lgkmcnt(0)
	s_barrier
	s_add_u32 s44, s44, s20
	ds_read2_b32 v[108:109], v86 offset0:129 offset1:133
	ds_read2_b32 v[110:111], v86 offset1:4
	ds_read2_b32 v[112:113], v98 offset0:2 offset1:6
	ds_read2_b32 v[114:115], v98 offset0:131 offset1:135
	ds_read2_b32 v[118:119], v99 offset0:4 offset1:8
	ds_read2_b32 v[120:121], v99 offset0:133 offset1:137
	s_addc_u32 s50, s50, 0
	s_add_u32 s18, s44, s18
	s_addc_u32 s19, s50, s19
	v_add_u32_e32 v100, 0xc00, v86
	s_add_u32 s18, s18, s45
	v_mov_b32_e32 v116, 0
	ds_read2_b32 v[122:123], v100 offset0:6 offset1:10
	ds_read2_b32 v[124:125], v100 offset0:135 offset1:139
	v_mov_b32_e32 v117, 0
	s_addc_u32 s19, s19, 0
	s_lshl_b64 s[2:3], s[2:3], 10
	s_addk_i32 s40, 0x4000
	s_waitcnt lgkmcnt(6)
	v_cvt_pk_fp8_f32 v116, v110, v108
	s_waitcnt lgkmcnt(2)
	v_cvt_pk_fp8_f32 v117, v118, v120
	s_add_u32 s40, s2, s40
	s_addc_u32 s44, s3, 0
	s_and_b64 s[2:3], exec, s[12:13]
	v_mov_b32_e32 v108, 0
	s_cselect_b32 s3, s44, s19
	s_cselect_b32 s2, s40, s18
	v_cvt_pk_fp8_f32 v116, v112, v114 op_sel:[0,0,1]
	s_waitcnt lgkmcnt(0)
	v_cvt_pk_fp8_f32 v117, v122, v124 op_sel:[0,0,1]
	v_cvt_pk_fp8_f32 v108, v111, v109
	v_mov_b32_e32 v109, 0
	v_lshl_add_u64 v[128:129], s[2:3], 0, v[72:73]
	v_cvt_pk_fp8_f32 v109, v119, v121
	v_lshl_add_u64 v[126:127], v[74:75], 0, s[4:5]
	v_lshlrev_b64 v[128:129], 10, v[128:129]
	v_lshl_add_u64 v[110:111], v[126:127], 0, v[128:129]
	global_store_dwordx2 v[110:111], v[116:117], off
	v_cvt_pk_fp8_f32 v108, v113, v115 op_sel:[0,0,1]
	v_cvt_pk_fp8_f32 v109, v123, v125 op_sel:[0,0,1]
	ds_read2_b32 v[112:113], v86 offset0:137 offset1:141
	ds_read2_b32 v[114:115], v98 offset0:10 offset1:14
	ds_read2_b32 v[116:117], v86 offset0:8 offset1:12
	ds_read2_b32 v[118:119], v98 offset0:139 offset1:143
	ds_read2_b32 v[122:123], v99 offset0:12 offset1:16
	ds_read2_b32 v[124:125], v99 offset0:141 offset1:145
	v_lshl_add_u64 v[110:111], s[2:3], 0, v[76:77]
	v_lshlrev_b64 v[110:111], 10, v[110:111]
	v_lshl_add_u64 v[110:111], v[126:127], 0, v[110:111]
	v_mov_b32_e32 v120, 0
	ds_read2_b32 v[128:129], v100 offset0:14 offset1:18
	ds_read2_b32 v[130:131], v100 offset0:143 offset1:147
	v_mov_b32_e32 v121, 0
	global_store_dwordx2 v[110:111], v[108:109], off
	v_mov_b32_e32 v110, v69
	v_mov_b32_e32 v111, v69
	s_waitcnt lgkmcnt(5)
	v_cvt_pk_fp8_f32 v120, v116, v112
	s_waitcnt lgkmcnt(2)
	v_cvt_pk_fp8_f32 v121, v122, v124
	v_cvt_pk_fp8_f32 v110, v117, v113
	v_cvt_pk_fp8_f32 v111, v123, v125
	v_cvt_pk_fp8_f32 v120, v114, v118 op_sel:[0,0,1]
	s_waitcnt lgkmcnt(0)
	v_cvt_pk_fp8_f32 v121, v128, v130 op_sel:[0,0,1]
	v_cvt_pk_fp8_f32 v110, v115, v119 op_sel:[0,0,1]
	v_cvt_pk_fp8_f32 v111, v129, v131 op_sel:[0,0,1]
	v_mov_b32_e32 v79, v69
	v_lshl_add_u64 v[108:109], s[2:3], 0, v[68:69]
	v_lshl_add_u64 v[78:79], s[2:3], 0, v[78:79]
	v_lshlrev_b64 v[108:109], 10, v[108:109]
	v_lshlrev_b64 v[78:79], 10, v[78:79]
	v_lshl_add_u64 v[108:109], v[126:127], 0, v[108:109]
	v_lshl_add_u64 v[78:79], v[126:127], 0, v[78:79]
	s_andn2_b64 vcc, exec, s[10:11]
	global_store_dwordx2 v[108:109], v[120:121], off
	global_store_dwordx2 v[78:79], v[110:111], off
	s_barrier
	s_cbranch_vccnz .LBB0_63
	s_add_i32 s40, s41, s92
	s_cmpk_gt_i32 s40, 0x17ff
	s_cbranch_scc1 .LBB0_87
	s_ashr_i32 s2, s40, 31
	s_lshr_b32 s2, s2, 21
	s_add_i32 s2, s40, s2
	s_and_b32 s2, s2, 0xfffff800
	s_sub_i32 s2, s40, s2
	s_ashr_i32 s2, s2, 6
	s_and_b32 s3, s40, 0xfffff800
	s_cmpk_eq_i32 s3, 0x800
	s_cselect_b32 s4, s86, s82
	s_cselect_b32 s10, s87, s83
	s_cmpk_eq_i32 s3, 0x1000
	s_cselect_b32 s10, s91, s10
	s_cselect_b32 s4, s90, s4
	s_ashr_i32 s3, s2, 31
	s_lshl_b64 s[2:3], s[2:3], 22
	s_add_u32 s2, s4, s2
	s_addc_u32 s3, s10, s3
	s_lshl_b32 s4, s40, 4
	s_and_b32 s4, s4, 0x380
	v_add_u32_e32 v68, s4, v67
	v_lshlrev_b64 v[2:3], 12, v[68:69]
	v_lshl_add_u64 v[2:3], s[2:3], 0, v[2:3]
	s_lshl_b32 s2, s40, 9
	s_and_b32 s4, s2, 0xe00
	v_lshl_add_u64 v[2:3], v[2:3], 0, s[4:5]
	v_mov_b32_e32 v71, v69
	v_lshl_add_u64 v[26:27], v[2:3], 0, v[70:71]
	v_add_co_u32_e32 v6, vcc, s21, v26
	s_nop 1
	v_addc_co_u32_e32 v7, vcc, 0, v27, vcc
	v_add_co_u32_e32 v10, vcc, s24, v26
	global_load_dwordx4 v[2:5], v[26:27], off nt
	s_nop 0
	global_load_dwordx4 v[6:9], v[6:7], off nt
	v_addc_co_u32_e32 v11, vcc, 0, v27, vcc
	v_add_co_u32_e32 v14, vcc, s25, v26
	s_nop 1
	v_addc_co_u32_e32 v15, vcc, 0, v27, vcc
	v_add_co_u32_e32 v18, vcc, s35, v26
	global_load_dwordx4 v[10:13], v[10:11], off nt
	s_nop 0
	global_load_dwordx4 v[14:17], v[14:15], off nt
	v_addc_co_u32_e32 v19, vcc, 0, v27, vcc
	v_add_co_u32_e32 v22, vcc, 0xa000, v26
	s_nop 1
	v_addc_co_u32_e32 v23, vcc, 0, v27, vcc
	v_add_co_u32_e32 v28, vcc, 0xc000, v26
	global_load_dwordx4 v[18:21], v[18:19], off nt
	s_nop 0
	global_load_dwordx4 v[22:25], v[22:23], off nt
	v_addc_co_u32_e32 v29, vcc, 0, v27, vcc
	v_add_co_u32_e32 v30, vcc, 0xe000, v26
	s_nop 1
	v_addc_co_u32_e32 v31, vcc, 0, v27, vcc
	global_load_dwordx4 v[26:29], v[28:29], off nt
	s_nop 0
	global_load_dwordx4 v[30:33], v[30:31], off nt

; #define GAS __attribute__((address_space(1)))
; __device__ __forceinline__ unsigned pk2(float lo, float hi) { return f2bf(lo) | (f2bf(hi) << 16); }
; __device__ __forceinline__ void p0_prologue(Frame& F, const Args& A) {
;     ...
;     { const float* wq = A.in[13]; const float* gx = A.in[11]; bf16* o = (bf16*)(ws + WS_WQ);
;       for (int i = (F.c * NTHREADS + F.tid); i < D * D / 8; i += F.G * NTHREADS) { const f32x4 a = *(const GAS f32x4*)(wq + 8 * (size_t)i), b2 = *(const GAS f32x4*)(wq + 8 * (size_t)i + 4); const float g = gx[i >> 7] * (1.0f / 16.0f);
;           *(GAS u32x4*)(o + 8 * (size_t)i) = (u32x4){pk2(a[0] * g, a[1] * g), pk2(a[2] * g, a[3] * g), pk2(b2[0] * g, b2[1] * g), pk2(b2[2] * g, b2[3] * g)}; } }
.LBB0_106:
	s_waitcnt vmcnt(4)
	v_ashrrev_i32_e32 v16, 7, v1
	v_ashrrev_i32_e32 v17, 31, v16
	v_lshl_add_u64 v[16:17], v[16:17], 2, s[42:43]
	global_load_dwordx4 v[8:11], v[4:5], off offset:-16 nt
	global_load_dwordx4 v[12:15], v[4:5], off nt
	global_load_dword v3, v[16:17], off
	v_add_u32_e32 v1, s2, v1
	v_cmp_lt_i32_e32 vcc, s13, v1
	v_lshl_add_u64 v[4:5], v[4:5], 0, s[6:7]
	s_or_b64 s[10:11], vcc, s[10:11]
	s_waitcnt vmcnt(2)
	v_mov_b32_e32 v16, v8
	v_mov_b32_e32 v17, v10
	v_mov_b32_e32 v10, v9
	s_waitcnt vmcnt(1)
	v_mov_b32_e32 v8, v12
	v_mov_b32_e32 v9, v14
	v_mov_b32_e32 v14, v13
	s_waitcnt vmcnt(0)
	v_mul_f32_e32 v12, 0x3d800000, v3
	v_pk_mul_f32 v[16:17], v[16:17], v[12:13] op_sel_hi:[1,0]
	v_pk_mul_f32 v[10:11], v[10:11], v[12:13] op_sel_hi:[1,0]
	v_pk_mul_f32 v[8:9], v[8:9], v[12:13] op_sel_hi:[1,0]
	v_pk_mul_f32 v[12:13], v[14:15], v[12:13] op_sel_hi:[1,0]
	v_bfe_u32 v15, v11, 16, 1
	v_bfe_u32 v14, v12, 16, 1
	v_bfe_u32 v18, v10, 16, 1
	v_bfe_u32 v19, v16, 16, 1
	v_bfe_u32 v20, v17, 16, 1
	v_bfe_u32 v21, v8, 16, 1
	v_bfe_u32 v22, v9, 16, 1
	v_bfe_u32 v3, v13, 16, 1
	v_add3_u32 v18, v10, v18, s3
	v_add3_u32 v15, v11, v15, s3
	v_add3_u32 v10, v12, v14, s3
	v_add3_u32 v9, v9, v22, s3
	v_add3_u32 v8, v8, v21, s3
	v_add3_u32 v11, v17, v20, s3
	v_add3_u32 v12, v16, v19, s3
	v_add3_u32 v3, v13, v3, s3
	v_lshrrev_b32_e32 v12, 16, v12
	v_lshrrev_b32_e32 v13, 16, v11
	v_lshrrev_b32_e32 v8, 16, v8
	v_lshrrev_b32_e32 v9, 16, v9
	v_and_or_b32 v11, v3, s12, v9
	v_and_or_b32 v10, v10, s12, v8
	v_and_or_b32 v9, v15, s12, v13
	v_and_or_b32 v8, v18, s12, v12
	global_store_dwordx4 v[6:7], v[8:11], off
	v_lshl_add_u64 v[6:7], v[6:7], 0, s[8:9]
	s_andn2_b64 exec, exec, s[10:11]
	s_cbranch_execnz .LBB0_106

; #define GAS __attribute__((address_space(1)))
; #define LAS __attribute__((address_space(3)))
; __device__ __forceinline__ void p0_transpose_item_i8(const float* W, int ldw, int csrc0, int k0, gu32* cmax, float* sbout, unsigned char* WT, int Kd, int drow0, LAS float* scr, int lane) {
;     { f32x4 v[8]; const int r8 = lane >> 3, c4 = (lane & 7) * 4;
; #pragma unroll
;       for (int i = 0; i < 8; ++i) v[i] = *(const GAS f32x4*)(W + (size_t)(k0 + 8 * i + r8) * ldw + csrc0 + c4);
;       f32x4 sc;
; #pragma unroll
;       for (int c = 0; c < 4; ++c) { const float mx = __builtin_bit_cast(float, __hip_atomic_load((unsigned*)(cmax + c4 + c), RLX_AGENT)); sc[c] = mx > 0.f ? 127.0f / mx : 0.f; if (k0 == 0 && r8 == 0) sbout[c4 + c] = mx * (1.0f / 127.0f); }
; #pragma unroll
;       for (int i = 0; i < 8; ++i) { const int kk = 8 * i + r8; scr[kk * 33 + c4] = v[i][0] * sc[0]; scr[kk * 33 + c4 + 1] = v[i][1] * sc[1]; scr[kk * 33 + c4 + 2] = v[i][2] * sc[2]; scr[kk * 33 + c4 + 3] = v[i][3] * sc[3]; } }
; __device__ __forceinline__ void p0_prologue(Frame& F, const Args& A) {
;     ...
;         else { const int r = it - I_IN, n0 = (r % 64) * 32; p0_transpose_item_i8(A.in[14], 2 * D, n0, (r / 64) * 64, cmax + NP + n0, (float*)(ws + WS_SBKV) + n0, ws + WS_WKV, D, n0, scr, lane); }
.LBB0_131:
	s_cmpk_gt_i32 s14, 0x4ff
	s_mov_b64 s[6:7], -1
	s_cbranch_scc0 .LBB0_136
	s_and_b32 s4, s14, 0x7fffffc0
	s_add_i32 s6, s4, 0xfffffb00
	s_and_b32 s18, s15, 0x7e0
	v_or_b32_e32 v66, s6, v167
	s_lshl_b32 s4, s18, 2
	s_waitcnt vmcnt(6)
	v_or_b32_e32 v6, 8, v66
	v_mov_b32_e32 v7, v67
	v_lshl_add_u64 v[2:3], v[44:45], 0, s[4:5]
	v_lshlrev_b64 v[4:5], 13, v[66:67]
	v_lshlrev_b64 v[6:7], 13, v[6:7]
	v_lshl_add_u64 v[4:5], v[2:3], 0, v[4:5]
	v_lshl_add_u64 v[6:7], v[2:3], 0, v[6:7]
	global_load_dwordx4 v[30:33], v[4:5], off nt
	global_load_dwordx4 v[18:21], v[6:7], off nt
	v_or_b32_e32 v4, 16, v66
	v_mov_b32_e32 v5, v67
	v_or_b32_e32 v6, 24, v66
	v_mov_b32_e32 v7, v67
	v_lshlrev_b64 v[4:5], 13, v[4:5]
	v_lshlrev_b64 v[6:7], 13, v[6:7]
	v_lshl_add_u64 v[4:5], v[2:3], 0, v[4:5]
	v_lshl_add_u64 v[6:7], v[2:3], 0, v[6:7]
	global_load_dwordx4 v[26:29], v[4:5], off nt
	global_load_dwordx4 v[10:13], v[6:7], off nt
	v_or_b32_e32 v4, 32, v66
	v_mov_b32_e32 v5, v67
	v_or_b32_e32 v6, 40, v66
	v_mov_b32_e32 v7, v67
	v_lshlrev_b64 v[4:5], 13, v[4:5]
	v_lshlrev_b64 v[6:7], 13, v[6:7]
	v_lshl_add_u64 v[4:5], v[2:3], 0, v[4:5]
	v_lshl_add_u64 v[6:7], v[2:3], 0, v[6:7]
	global_load_dwordx4 v[22:25], v[4:5], off nt
	s_nop 0
	global_load_dwordx4 v[6:9], v[6:7], off nt
	v_or_b32_e32 v4, 48, v66
	v_mov_b32_e32 v5, v67
	v_or_b32_e32 v66, 56, v66
	v_lshlrev_b64 v[4:5], 13, v[4:5]
	s_waitcnt vmcnt(10)
	v_lshlrev_b64 v[14:15], 13, v[66:67]
	v_lshl_add_u64 v[4:5], v[2:3], 0, v[4:5]
	v_lshl_add_u64 v[2:3], v[2:3], 0, v[14:15]
	v_lshl_add_u64 v[48:49], v[36:37], 0, s[4:5]
	global_load_dwordx4 v[14:17], v[4:5], off nt
	s_nop 0
	global_load_dwordx4 v[2:5], v[2:3], off nt
	s_add_u32 s8, s20, s4
	global_load_dword v51, v[48:49], off sc1
	s_addc_u32 s9, s21, 0
	s_cmp_eq_u32 s6, 0
	s_cselect_b64 s[10:11], -1, 0
	s_and_b64 s[10:11], s[10:11], s[2:3]
	s_and_saveexec_b64 s[12:13], s[10:11]
	s_cbranch_execz .LBB0_137
	v_lshlrev_b32_e32 v52, 2, v34
	s_waitcnt vmcnt(0)
	v_mul_f32_e32 v53, 0x3c010204, v51
	global_store_dword v52, v53, s[8:9]
	s_or_b64 exec, exec, s[12:13]
	global_load_dword v52, v[48:49], off offset:4 sc1
	s_and_saveexec_b64 s[12:13], s[10:11]
	s_cbranch_execnz .LBB0_138

; #define GAS __attribute__((address_space(1)))
; #define LAS __attribute__((address_space(3)))
; __device__ __forceinline__ void p0_transpose_item_i8(const float* W, int ldw, int csrc0, int k0, gu32* cmax, float* sbout, unsigned char* WT, int Kd, int drow0, LAS float* scr, int lane) {
;     { f32x4 v[8]; const int r8 = lane >> 3, c4 = (lane & 7) * 4;
; #pragma unroll
;       for (int i = 0; i < 8; ++i) v[i] = *(const GAS f32x4*)(W + (size_t)(k0 + 8 * i + r8) * ldw + csrc0 + c4);
;       f32x4 sc;
; #pragma unroll
;       for (int c = 0; c < 4; ++c) { const float mx = __builtin_bit_cast(float, __hip_atomic_load((unsigned*)(cmax + c4 + c), RLX_AGENT)); sc[c] = mx > 0.f ? 127.0f / mx : 0.f; if (k0 == 0 && r8 == 0) sbout[c4 + c] = mx * (1.0f / 127.0f); }
; #pragma unroll
;       for (int i = 0; i < 8; ++i) { const int kk = 8 * i + r8; scr[kk * 33 + c4] = v[i][0] * sc[0]; scr[kk * 33 + c4 + 1] = v[i][1] * sc[1]; scr[kk * 33 + c4 + 2] = v[i][2] * sc[2]; scr[kk * 33 + c4 + 3] = v[i][3] * sc[3]; } }
; __device__ __forceinline__ void p0_prologue(Frame& F, const Args& A) {
;     ...
;         if (it < I_IN) { const int kb = it / (NP / 32), nb = it % (NP / 32), n0 = nb * 32; p0_transpose_item_i8(A.in[3], INW, n0 + (n0 >= 1536 ? 8 : 0), kb * 64, cmax + n0, (float*)(ws + WS_SB) + n0, ws + WS_WIN, D, n0, scr, lane); }
.LBB0_142:
	s_mul_hi_i32 s4, s14, 0x66666667
	s_lshr_b32 s6, s4, 31
	s_ashr_i32 s4, s4, 5
	s_add_i32 s4, s4, s6
	s_mul_i32 s6, s4, 0xffffffb0
	s_add_i32 s7, s14, s6
	s_mul_i32 s6, s4, 0xfffff600
	s_add_i32 s6, s15, s6
	s_cmp_gt_i32 s7, 47
	s_cselect_b32 s7, 8, 0
	s_mul_i32 s8, s4, 0xa00
	s_sub_i32 s7, s7, s8
	s_add_i32 s12, s15, s7
	s_ashr_i32 s7, s6, 31
	s_lshl_b32 s8, s4, 6
	s_lshl_b64 s[18:19], s[6:7], 2
	s_add_u32 s10, s24, s18
	s_addc_u32 s11, s25, s19
	s_waitcnt vmcnt(6)
	v_or_b32_e32 v8, s8, v167
	s_ashr_i32 s13, s12, 31
	v_lshl_add_u64 v[2:3], s[12:13], 2, v[46:47]
	v_or_b32_e32 v6, 8, v8
	v_mad_i64_i32 v[4:5], s[12:13], v8, s41, v[2:3]
	v_mad_i64_i32 v[6:7], s[12:13], v6, s41, v[2:3]
	global_load_dwordx4 v[30:33], v[4:5], off nt
	global_load_dwordx4 v[26:29], v[6:7], off nt
	v_or_b32_e32 v4, 16, v8
	v_or_b32_e32 v6, 24, v8
	v_mad_i64_i32 v[4:5], s[12:13], v4, s41, v[2:3]
	v_mad_i64_i32 v[6:7], s[12:13], v6, s41, v[2:3]
	global_load_dwordx4 v[22:25], v[4:5], off nt
	global_load_dwordx4 v[18:21], v[6:7], off nt
	v_or_b32_e32 v4, 32, v8
	v_or_b32_e32 v6, 40, v8
	v_mad_i64_i32 v[4:5], s[12:13], v4, s41, v[2:3]
	v_mad_i64_i32 v[6:7], s[12:13], v6, s41, v[2:3]
	global_load_dwordx4 v[14:17], v[4:5], off nt
	global_load_dwordx4 v[10:13], v[6:7], off nt
	v_or_b32_e32 v4, 48, v8
	v_or_b32_e32 v6, 56, v8
	v_mad_i64_i32 v[4:5], s[12:13], v4, s41, v[2:3]
	v_mad_i64_i32 v[2:3], s[12:13], v6, s41, v[2:3]
	v_lshl_add_u64 v[48:49], v[40:41], 0, s[18:19]
	global_load_dwordx4 v[6:9], v[4:5], off nt
	s_nop 0
	global_load_dwordx4 v[2:5], v[2:3], off nt
	s_add_i32 s4, s14, 0x4f
	global_load_dword v51, v[48:49], off sc1
	s_cmpk_lt_u32 s4, 0x9f
	s_cselect_b64 s[12:13], -1, 0
	s_and_b64 s[12:13], s[12:13], s[2:3]
	v_lshlrev_b32_e32 v54, 2, v34
	s_and_saveexec_b64 s[18:19], s[12:13]
	s_cbranch_execz .LBB0_146
	s_waitcnt vmcnt(0)
	v_mul_f32_e32 v52, 0x3c010204, v51
	global_store_dword v54, v52, s[10:11]
	s_or_b64 exec, exec, s[18:19]
	global_load_dword v52, v[48:49], off offset:4 sc1
	s_and_saveexec_b64 s[18:19], s[12:13]
	s_cbranch_execnz .LBB0_147
